# LDS-read hoist register pool narrowed to v<224 in the attention MFMA segments
# speedup vs baseline: 1.0003x; 1.0003x over previous
.LBB0_528:
	ds_read_b128 v[88:91], v129
	ds_read_b128 v[92:95], v129 offset:1024
	ds_read_b128 v[96:99], v130
	ds_read_b128 v[152:155], v130 offset:1024
	ds_read_b128 v[176:179], v131
	ds_read_b128 v[180:183], v131 offset:1024
	ds_read_b128 v[184:187], v132
	ds_read_b128 v[188:191], v132 offset:1024
	ds_read_b128 v[192:195], v129 offset:8192
	ds_read_b128 v[196:199], v129 offset:9216
	ds_read_b128 v[200:203], v130 offset:8192
	ds_read_b128 v[204:207], v130 offset:9216
	ds_read_b128 v[208:211], v131 offset:8192
	ds_read_b128 v[212:215], v131 offset:9216
	ds_read_b128 v[216:219], v132 offset:8192
	s_and_b64 vcc, exec, s[10:11]
	s_waitcnt lgkmcnt(11)
	v_mfma_f32_16x16x32_bf16 v[72:75], v[88:91], v[0:3], v[240:243]
	ds_read_b128 v[220:223], v132 offset:9216
	ds_read_b64_tr_b16 v[88:89], v142 offset:49152
	ds_read_b64_tr_b16 v[90:91], v146 offset:49152
	v_mfma_f32_16x16x32_bf16 v[72:75], v[96:99], v[4:7], v[72:75]
	ds_read_b64_tr_b16 v[98:99], v146 offset:57344
	v_mfma_f32_16x16x32_bf16 v[76:79], v[92:95], v[0:3], v[240:243]
	s_waitcnt lgkmcnt(11)
	v_mfma_f32_16x16x32_bf16 v[72:75], v[176:179], v[8:11], v[72:75]
	ds_read_b64_tr_b16 v[96:97], v142 offset:57344
	ds_read_b64_tr_b16 v[92:93], v136 offset:49152
	ds_read_b64_tr_b16 v[94:95], v137 offset:49152
	ds_read_b64_tr_b16 v[178:179], v137 offset:57344
	v_mfma_f32_16x16x32_bf16 v[84:87], v[184:187], v[12:15], v[72:75]
	v_mfma_f32_16x16x32_bf16 v[72:75], v[152:155], v[4:7], v[76:79]
	v_mfma_f32_16x16x32_bf16 v[72:75], v[180:183], v[8:11], v[72:75]
	v_mfma_f32_16x16x32_bf16 v[80:83], v[188:191], v[12:15], v[72:75]
	s_waitcnt lgkmcnt(11)
	s_nop 5
	v_mfma_f32_16x16x32_bf16 v[72:75], v[192:195], v[0:3], v[240:243]
	ds_read_b64_tr_b16 v[176:177], v136 offset:57344
	ds_read_b64_tr_b16 v[184:185], v139 offset:49152
	ds_read_b64_tr_b16 v[186:187], v145 offset:49152
	ds_read_b64_tr_b16 v[154:155], v145 offset:57344
	v_mfma_f32_16x16x32_bf16 v[72:75], v[200:203], v[4:7], v[72:75]
	s_waitcnt lgkmcnt(11)
	v_mfma_f32_16x16x32_bf16 v[72:75], v[208:211], v[8:11], v[72:75]
	ds_read_b64_tr_b16 v[152:153], v139 offset:57344
	ds_read_b64_tr_b16 v[180:181], v140 offset:49152
	ds_read_b64_tr_b16 v[182:183], v147 offset:49152
	ds_read_b64_tr_b16 v[190:191], v147 offset:57344
	v_mfma_f32_16x16x32_bf16 v[76:79], v[216:219], v[12:15], v[72:75]
	v_mfma_f32_16x16x32_bf16 v[72:75], v[196:199], v[0:3], v[240:243]
	v_mfma_f32_16x16x32_bf16 v[72:75], v[204:207], v[4:7], v[72:75]
	s_waitcnt lgkmcnt(10)
	v_mfma_f32_16x16x32_bf16 v[60:63], v[88:91], v[68:71], v[60:63]
	ds_read_b64_tr_b16 v[188:189], v140 offset:57344
	ds_read_b64_tr_b16 v[192:193], v148 offset:49152
	ds_read_b64_tr_b16 v[194:195], v149 offset:49152
	ds_read_b64_tr_b16 v[202:203], v149 offset:57344
	ds_read_b64_tr_b16 v[200:201], v148 offset:57344
	v_mfma_f32_16x16x32_bf16 v[60:63], v[96:99], v[64:67], v[60:63]
	s_waitcnt lgkmcnt(11)
	v_mfma_f32_16x16x32_bf16 v[52:55], v[92:95], v[68:71], v[52:55]
	ds_read_b64_tr_b16 v[208:209], v133 offset:49152
	ds_read_b64_tr_b16 v[210:211], v134 offset:49152
	ds_read_b64_tr_b16 v[218:219], v134 offset:57344
	ds_read_b64_tr_b16 v[216:217], v133 offset:57344
	v_mfma_f32_16x16x32_bf16 v[52:55], v[176:179], v[64:67], v[52:55]
	s_waitcnt lgkmcnt(11)
	v_mfma_f32_16x16x32_bf16 v[48:51], v[184:187], v[68:71], v[48:51]
	ds_read_b64_tr_b16 v[196:197], v135 offset:49152
	ds_read_b64_tr_b16 v[198:199], v138 offset:49152
	ds_read_b64_tr_b16 v[206:207], v138 offset:57344
	ds_read_b64_tr_b16 v[204:205], v135 offset:57344
	v_mfma_f32_16x16x32_bf16 v[48:51], v[152:155], v[64:67], v[48:51]
	s_waitcnt lgkmcnt(11)
	v_mfma_f32_16x16x32_bf16 v[56:59], v[180:183], v[68:71], v[56:59]
	ds_read_b64_tr_b16 v[88:89], v141 offset:49152
	ds_read_b64_tr_b16 v[90:91], v143 offset:49152
	ds_read_b64_tr_b16 v[98:99], v143 offset:57344
	ds_read_b64_tr_b16 v[96:97], v141 offset:57344
	v_mfma_f32_16x16x32_bf16 v[56:59], v[188:191], v[64:67], v[56:59]
	s_waitcnt lgkmcnt(11)
	v_mfma_f32_16x16x32_bf16 v[32:35], v[192:195], v[68:71], v[32:35]
	v_mfma_f32_16x16x32_bf16 v[32:35], v[200:203], v[64:67], v[32:35]
	s_waitcnt lgkmcnt(7)
	v_mfma_f32_16x16x32_bf16 v[36:39], v[208:211], v[68:71], v[36:39]
	v_mfma_f32_16x16x32_bf16 v[36:39], v[216:219], v[64:67], v[36:39]
	s_waitcnt lgkmcnt(3)
	v_mfma_f32_16x16x32_bf16 v[40:43], v[196:199], v[68:71], v[40:43]
	v_mfma_f32_16x16x32_bf16 v[40:43], v[204:207], v[64:67], v[40:43]
	v_mfma_f32_16x16x32_bf16 v[72:75], v[212:215], v[8:11], v[72:75]
	s_waitcnt lgkmcnt(0)
	v_mfma_f32_16x16x32_bf16 v[44:47], v[88:91], v[68:71], v[44:47]
	v_mfma_f32_16x16x32_bf16 v[72:75], v[220:223], v[12:15], v[72:75]
	v_mfma_f32_16x16x32_bf16 v[44:47], v[96:99], v[64:67], v[44:47]
	s_cbranch_vccnz .LBB0_530
	v_add_u32_e32 v64, 0, v109
	s_waitcnt vmcnt(3)
	ds_write_b128 v100, v[16:19] offset:16384
	s_waitcnt vmcnt(2)
	ds_write_b128 v124, v[20:23] offset:16384
	s_waitcnt vmcnt(1)
	ds_write_b128 v64, v[24:27] offset:32768
	v_add_u32_e32 v64, 0, v112
	s_waitcnt vmcnt(0)
	ds_write_b128 v64, v[28:31] offset:32768

.LBB0_536:
	ds_read_b128 v[168:171], v129 offset:16384
	ds_read_b128 v[172:175], v130 offset:16384
	ds_read_b128 v[176:179], v131 offset:16384
	ds_read_b128 v[180:183], v129 offset:17408
	ds_read_b128 v[184:187], v132 offset:16384
	ds_read_b128 v[188:191], v130 offset:17408
	ds_read_b128 v[192:195], v131 offset:17408
	ds_read_b128 v[196:199], v129 offset:24576
	ds_read_b128 v[200:203], v132 offset:17408
	ds_read_b128 v[204:207], v130 offset:24576
	ds_read_b128 v[208:211], v131 offset:24576
	ds_read_b128 v[212:215], v129 offset:25600
	ds_read_b128 v[216:219], v132 offset:24576
	ds_read_b128 v[220:223], v130 offset:25600
	v_sub_f32_e32 v64, v84, v96
	v_exp_f32_e32 v96, v64
	v_sub_f32_e32 v64, v85, v97
	v_exp_f32_e32 v97, v64
	v_sub_f32_e32 v64, v86, v98
	v_exp_f32_e32 v98, v64
	v_sub_f32_e32 v64, v87, v99
	v_exp_f32_e32 v99, v64
	v_sub_f32_e32 v64, v80, v92
	v_exp_f32_e32 v153, v64
	v_sub_f32_e32 v64, v81, v93
	v_exp_f32_e32 v154, v64
	v_sub_f32_e32 v64, v82, v94
	v_exp_f32_e32 v155, v64
	v_sub_f32_e32 v64, v83, v95
	s_waitcnt lgkmcnt(10)
	v_mfma_f32_16x16x32_bf16 v[84:87], v[168:171], v[0:3], v[240:243]
	ds_read_b128 v[168:171], v131 offset:25600
	v_exp_f32_e32 v156, v64
	v_sub_f32_e32 v64, v76, v88
	v_exp_f32_e32 v157, v64
	v_mfma_f32_16x16x32_bf16 v[92:95], v[180:183], v[0:3], v[240:243]
	ds_read_b128 v[180:183], v132 offset:25600
	v_sub_f32_e32 v64, v77, v89
	v_sub_f32_e32 v70, v73, v67
	v_mfma_f32_16x16x32_bf16 v[84:87], v[172:175], v[4:7], v[84:87]
	ds_read_b64_tr_b16 v[172:173], v142 offset:32768
	ds_read_b64_tr_b16 v[174:175], v146 offset:32768
	v_exp_f32_e32 v158, v64
	v_sub_f32_e32 v64, v78, v90
	v_exp_f32_e32 v159, v64
	v_sub_f32_e32 v64, v79, v91
	s_waitcnt lgkmcnt(9)
	v_mfma_f32_16x16x32_bf16 v[88:91], v[188:191], v[4:7], v[92:95]
	ds_read_b64_tr_b16 v[190:191], v146 offset:40960
	ds_read_b64_tr_b16 v[188:189], v142 offset:40960
	v_exp_f32_e32 v160, v64
	v_mfma_f32_16x16x32_bf16 v[80:83], v[176:179], v[8:11], v[84:87]
	ds_read_b64_tr_b16 v[176:177], v136 offset:32768
	ds_read_b64_tr_b16 v[178:179], v137 offset:32768
	v_sub_f32_e32 v64, v72, v66
	v_exp_f32_e32 v161, v64
	v_mfma_f32_16x16x32_bf16 v[76:79], v[192:195], v[8:11], v[88:91]
	ds_read_b64_tr_b16 v[194:195], v137 offset:40960
	ds_read_b64_tr_b16 v[192:193], v136 offset:40960
	v_sub_f32_e32 v68, v74, v68
	s_and_b64 vcc, exec, s[10:11]
	v_mfma_f32_16x16x32_bf16 v[92:95], v[196:199], v[0:3], v[240:243]
	v_mfma_f32_16x16x32_bf16 v[80:83], v[184:187], v[12:15], v[80:83]
	v_exp_f32_e32 v162, v70
	v_exp_f32_e32 v163, v68
	v_mfma_f32_16x16x32_bf16 v[76:79], v[200:203], v[12:15], v[76:79]
	s_waitcnt lgkmcnt(11)
	v_mfma_f32_16x16x32_bf16 v[88:91], v[204:207], v[4:7], v[92:95]
	ds_read_b64_tr_b16 v[196:197], v139 offset:32768
	ds_read_b64_tr_b16 v[198:199], v145 offset:32768
	ds_read_b64_tr_b16 v[186:187], v145 offset:40960
	ds_read_b64_tr_b16 v[184:185], v139 offset:40960
	v_sub_f32_e32 v68, v75, v69
	v_mfma_f32_16x16x32_bf16 v[84:87], v[208:211], v[8:11], v[88:91]
	v_cvt_pk_bf16_f32 v92, v96, v97
	v_cvt_pk_bf16_f32 v93, v98, v99
	v_cvt_pk_bf16_f32 v94, v153, v154
	v_mfma_f32_16x16x32_bf16 v[64:67], v[216:219], v[12:15], v[84:87]
	v_cvt_pk_bf16_f32 v95, v155, v156
	v_mfma_f32_16x16x32_bf16 v[84:87], v[212:215], v[0:3], v[240:243]
	v_exp_f32_e32 v164, v68
	s_waitcnt lgkmcnt(11)
	v_mfma_f32_16x16x32_bf16 v[84:87], v[220:223], v[4:7], v[84:87]
	ds_read_b64_tr_b16 v[200:201], v140 offset:32768
	ds_read_b64_tr_b16 v[202:203], v147 offset:32768
	ds_read_b64_tr_b16 v[206:207], v147 offset:40960
	ds_read_b64_tr_b16 v[204:205], v140 offset:40960
	v_mfma_f32_16x16x32_bf16 v[68:71], v[168:171], v[8:11], v[84:87]
	s_nop 2
	v_cvt_pk_bf16_f32 v84, v157, v158
	v_mfma_f32_16x16x32_bf16 v[68:71], v[180:183], v[12:15], v[68:71]
	v_cvt_pk_bf16_f32 v85, v159, v160
	v_cvt_pk_bf16_f32 v86, v161, v162
	s_waitcnt lgkmcnt(11)
	v_mfma_f32_16x16x32_bf16 v[60:63], v[172:175], v[92:95], v[60:63]
	ds_read_b64_tr_b16 v[208:209], v148 offset:32768
	ds_read_b64_tr_b16 v[210:211], v149 offset:32768
	ds_read_b64_tr_b16 v[218:219], v149 offset:40960
	ds_read_b64_tr_b16 v[216:217], v148 offset:40960
	v_cvt_pk_bf16_f32 v87, v163, v164
	s_nop 1
	v_mfma_f32_16x16x32_bf16 v[60:63], v[188:191], v[84:87], v[60:63]
	s_waitcnt lgkmcnt(11)
	v_mfma_f32_16x16x32_bf16 v[52:55], v[176:179], v[92:95], v[52:55]
	ds_read_b64_tr_b16 v[212:213], v133 offset:32768
	ds_read_b64_tr_b16 v[214:215], v134 offset:32768
	ds_read_b64_tr_b16 v[222:223], v134 offset:40960
	ds_read_b64_tr_b16 v[220:221], v133 offset:40960
	v_mfma_f32_16x16x32_bf16 v[52:55], v[192:195], v[84:87], v[52:55]
	s_waitcnt lgkmcnt(11)
	v_mfma_f32_16x16x32_bf16 v[48:51], v[196:199], v[92:95], v[48:51]
	ds_read_b64_tr_b16 v[168:169], v135 offset:32768
	ds_read_b64_tr_b16 v[170:171], v138 offset:32768
	ds_read_b64_tr_b16 v[182:183], v138 offset:40960
	ds_read_b64_tr_b16 v[180:181], v135 offset:40960
	v_mfma_f32_16x16x32_bf16 v[48:51], v[184:187], v[84:87], v[48:51]
	s_waitcnt lgkmcnt(11)
	v_mfma_f32_16x16x32_bf16 v[56:59], v[200:203], v[92:95], v[56:59]
	ds_read_b64_tr_b16 v[172:173], v141 offset:32768
	ds_read_b64_tr_b16 v[174:175], v143 offset:32768
	ds_read_b64_tr_b16 v[190:191], v143 offset:40960
	ds_read_b64_tr_b16 v[188:189], v141 offset:40960
	v_mfma_f32_16x16x32_bf16 v[56:59], v[204:207], v[84:87], v[56:59]
	s_waitcnt lgkmcnt(11)
	v_mfma_f32_16x16x32_bf16 v[32:35], v[208:211], v[92:95], v[32:35]
	v_mfma_f32_16x16x32_bf16 v[32:35], v[216:219], v[84:87], v[32:35]
	s_waitcnt lgkmcnt(7)
	v_mfma_f32_16x16x32_bf16 v[36:39], v[212:215], v[92:95], v[36:39]
	v_mfma_f32_16x16x32_bf16 v[36:39], v[220:223], v[84:87], v[36:39]
	s_waitcnt lgkmcnt(3)
	v_mfma_f32_16x16x32_bf16 v[40:43], v[168:171], v[92:95], v[40:43]
	v_mfma_f32_16x16x32_bf16 v[40:43], v[180:183], v[84:87], v[40:43]
	s_waitcnt lgkmcnt(0)
	v_mfma_f32_16x16x32_bf16 v[44:47], v[172:175], v[92:95], v[44:47]
	v_mfma_f32_16x16x32_bf16 v[44:47], v[188:191], v[84:87], v[44:47]
	s_cbranch_vccnz .LBB0_538
	v_add_u32_e32 v72, 0, v109
	s_waitcnt vmcnt(3)
	ds_write_b128 v100, v[16:19]
	s_waitcnt vmcnt(2)
	ds_write_b128 v124, v[20:23]
	s_waitcnt vmcnt(1)
	ds_write_b128 v72, v[24:27] offset:49152
	v_add_u32_e32 v72, 0, v112
	s_waitcnt vmcnt(0)
	ds_write_b128 v72, v[28:31] offset:49152

.LBB0_567:
	ds_read_b128 v[88:91], v129
	ds_read_b128 v[92:95], v129 offset:1024
	ds_read_b128 v[96:99], v130
	ds_read_b128 v[152:155], v130 offset:1024
	ds_read_b128 v[172:175], v131
	ds_read_b128 v[176:179], v131 offset:1024
	ds_read_b128 v[180:183], v132
	ds_read_b128 v[184:187], v132 offset:1024
	ds_read_b128 v[188:191], v129 offset:8192
	ds_read_b128 v[192:195], v129 offset:9216
	ds_read_b128 v[196:199], v130 offset:8192
	ds_read_b128 v[200:203], v130 offset:9216
	ds_read_b128 v[204:207], v131 offset:8192
	ds_read_b128 v[208:211], v131 offset:9216
	ds_read_b128 v[212:215], v132 offset:8192
	s_and_b64 vcc, exec, s[10:11]
	s_waitcnt lgkmcnt(11)
	v_mfma_f32_16x16x32_bf16 v[72:75], v[88:91], v[0:3], v[240:243]
	ds_read_b128 v[216:219], v132 offset:9216
	ds_read_b64_tr_b16 v[220:221], v146 offset:49152
	ds_read_b64_tr_b16 v[222:223], v148 offset:49152
	ds_read_b64_tr_b16 v[90:91], v148 offset:57344
	v_mfma_f32_16x16x32_bf16 v[72:75], v[96:99], v[4:7], v[72:75]
	v_mfma_f32_16x16x32_bf16 v[76:79], v[92:95], v[0:3], v[240:243]
	s_waitcnt lgkmcnt(11)
	v_mfma_f32_16x16x32_bf16 v[72:75], v[172:175], v[8:11], v[72:75]
	ds_read_b64_tr_b16 v[88:89], v146 offset:57344
	ds_read_b64_tr_b16 v[96:97], v139 offset:49152
	ds_read_b64_tr_b16 v[98:99], v142 offset:49152
	ds_read_b64_tr_b16 v[94:95], v142 offset:57344
	v_mfma_f32_16x16x32_bf16 v[84:87], v[180:183], v[12:15], v[72:75]
	v_mfma_f32_16x16x32_bf16 v[72:75], v[152:155], v[4:7], v[76:79]
	v_mfma_f32_16x16x32_bf16 v[72:75], v[176:179], v[8:11], v[72:75]
	v_mfma_f32_16x16x32_bf16 v[80:83], v[184:187], v[12:15], v[72:75]
	s_waitcnt lgkmcnt(11)
	s_nop 5
	v_mfma_f32_16x16x32_bf16 v[72:75], v[188:191], v[0:3], v[240:243]
	ds_read_b64_tr_b16 v[92:93], v139 offset:57344
	ds_read_b64_tr_b16 v[172:173], v141 offset:49152
	ds_read_b64_tr_b16 v[174:175], v145 offset:49152
	ds_read_b64_tr_b16 v[182:183], v145 offset:57344
	v_mfma_f32_16x16x32_bf16 v[72:75], v[196:199], v[4:7], v[72:75]
	s_waitcnt lgkmcnt(11)
	v_mfma_f32_16x16x32_bf16 v[72:75], v[204:207], v[8:11], v[72:75]
	ds_read_b64_tr_b16 v[180:181], v141 offset:57344
	ds_read_b64_tr_b16 v[152:153], v140 offset:49152
	ds_read_b64_tr_b16 v[154:155], v143 offset:49152
	ds_read_b64_tr_b16 v[178:179], v143 offset:57344
	v_mfma_f32_16x16x32_bf16 v[76:79], v[212:215], v[12:15], v[72:75]
	v_mfma_f32_16x16x32_bf16 v[72:75], v[192:195], v[0:3], v[240:243]
	v_mfma_f32_16x16x32_bf16 v[72:75], v[200:203], v[4:7], v[72:75]
	s_waitcnt lgkmcnt(10)
	v_mfma_f32_16x16x32_bf16 v[60:63], v[220:223], v[68:71], v[60:63]
	ds_read_b64_tr_b16 v[176:177], v140 offset:57344
	ds_read_b64_tr_b16 v[184:185], v147 offset:49152
	ds_read_b64_tr_b16 v[186:187], v149 offset:49152
	ds_read_b64_tr_b16 v[190:191], v149 offset:57344
	ds_read_b64_tr_b16 v[188:189], v147 offset:57344
	v_mfma_f32_16x16x32_bf16 v[60:63], v[88:91], v[64:67], v[60:63]
	s_waitcnt lgkmcnt(11)
	v_mfma_f32_16x16x32_bf16 v[56:59], v[96:99], v[68:71], v[56:59]
	ds_read_b64_tr_b16 v[196:197], v133 offset:49152
	ds_read_b64_tr_b16 v[198:199], v134 offset:49152
	ds_read_b64_tr_b16 v[206:207], v134 offset:57344
	ds_read_b64_tr_b16 v[204:205], v133 offset:57344
	v_mfma_f32_16x16x32_bf16 v[56:59], v[92:95], v[64:67], v[56:59]
	s_waitcnt lgkmcnt(11)
	v_mfma_f32_16x16x32_bf16 v[52:55], v[172:175], v[68:71], v[52:55]
	ds_read_b64_tr_b16 v[212:213], v135 offset:49152
	ds_read_b64_tr_b16 v[214:215], v136 offset:49152
	ds_read_b64_tr_b16 v[194:195], v136 offset:57344
	ds_read_b64_tr_b16 v[192:193], v135 offset:57344
	v_mfma_f32_16x16x32_bf16 v[52:55], v[180:183], v[64:67], v[52:55]
	s_waitcnt lgkmcnt(11)
	v_mfma_f32_16x16x32_bf16 v[48:51], v[152:155], v[68:71], v[48:51]
	ds_read_b64_tr_b16 v[200:201], v137 offset:49152
	ds_read_b64_tr_b16 v[202:203], v138 offset:49152
	ds_read_b64_tr_b16 v[222:223], v138 offset:57344
	ds_read_b64_tr_b16 v[220:221], v137 offset:57344
	v_mfma_f32_16x16x32_bf16 v[48:51], v[176:179], v[64:67], v[48:51]
	s_waitcnt lgkmcnt(11)
	v_mfma_f32_16x16x32_bf16 v[32:35], v[184:187], v[68:71], v[32:35]
	v_mfma_f32_16x16x32_bf16 v[32:35], v[188:191], v[64:67], v[32:35]
	s_waitcnt lgkmcnt(7)
	v_mfma_f32_16x16x32_bf16 v[36:39], v[196:199], v[68:71], v[36:39]
	v_mfma_f32_16x16x32_bf16 v[36:39], v[204:207], v[64:67], v[36:39]
	s_waitcnt lgkmcnt(3)
	v_mfma_f32_16x16x32_bf16 v[40:43], v[212:215], v[68:71], v[40:43]
	v_mfma_f32_16x16x32_bf16 v[40:43], v[192:195], v[64:67], v[40:43]
	v_mfma_f32_16x16x32_bf16 v[72:75], v[208:211], v[8:11], v[72:75]
	s_waitcnt lgkmcnt(0)
	v_mfma_f32_16x16x32_bf16 v[44:47], v[200:203], v[68:71], v[44:47]
	v_mfma_f32_16x16x32_bf16 v[72:75], v[216:219], v[12:15], v[72:75]
	v_mfma_f32_16x16x32_bf16 v[44:47], v[220:223], v[64:67], v[44:47]
	s_cbranch_vccnz .LBB0_569
	v_add_u32_e32 v64, 0, v109
	s_waitcnt vmcnt(3)
	ds_write_b128 v100, v[16:19] offset:16384
	s_waitcnt vmcnt(2)
	ds_write_b128 v124, v[20:23] offset:16384
	s_waitcnt vmcnt(1)
	ds_write_b128 v64, v[24:27] offset:32768
	v_add_u32_e32 v64, 0, v112
	s_waitcnt vmcnt(0)
	ds_write_b128 v64, v[28:31] offset:32768

.LBB0_575:
	ds_read_b128 v[164:167], v129 offset:16384
	ds_read_b128 v[168:171], v130 offset:16384
	ds_read_b128 v[172:175], v131 offset:16384
	ds_read_b128 v[176:179], v129 offset:17408
	ds_read_b128 v[180:183], v132 offset:16384
	ds_read_b128 v[184:187], v130 offset:17408
	ds_read_b128 v[188:191], v131 offset:17408
	ds_read_b128 v[192:195], v129 offset:24576
	ds_read_b128 v[196:199], v132 offset:17408
	ds_read_b128 v[200:203], v130 offset:24576
	ds_read_b128 v[204:207], v131 offset:24576
	ds_read_b128 v[208:211], v129 offset:25600
	ds_read_b128 v[212:215], v132 offset:24576
	ds_read_b128 v[216:219], v130 offset:25600
	ds_read_b128 v[220:223], v131 offset:25600
	v_sub_f32_e32 v64, v84, v96
	v_exp_f32_e32 v96, v64
	v_sub_f32_e32 v64, v85, v97
	v_exp_f32_e32 v97, v64
	v_sub_f32_e32 v64, v86, v98
	v_exp_f32_e32 v98, v64
	v_sub_f32_e32 v64, v87, v99
	v_exp_f32_e32 v99, v64
	v_sub_f32_e32 v64, v80, v92
	v_exp_f32_e32 v152, v64
	v_sub_f32_e32 v64, v81, v93
	v_exp_f32_e32 v153, v64
	v_sub_f32_e32 v64, v82, v94
	v_exp_f32_e32 v154, v64
	v_sub_f32_e32 v64, v83, v95
	s_waitcnt lgkmcnt(11)
	v_mfma_f32_16x16x32_bf16 v[84:87], v[164:167], v[0:3], v[240:243]
	ds_read_b128 v[164:167], v132 offset:25600
	v_exp_f32_e32 v155, v64
	v_sub_f32_e32 v64, v76, v88
	v_mfma_f32_16x16x32_bf16 v[84:87], v[168:171], v[4:7], v[84:87]
	ds_read_b64_tr_b16 v[168:169], v146 offset:32768
	ds_read_b64_tr_b16 v[170:171], v148 offset:32768
	v_exp_f32_e32 v156, v64
	v_sub_f32_e32 v64, v77, v89
	v_mfma_f32_16x16x32_bf16 v[92:95], v[176:179], v[0:3], v[240:243]
	ds_read_b64_tr_b16 v[178:179], v148 offset:40960
	v_exp_f32_e32 v157, v64
	v_sub_f32_e32 v64, v78, v90
	v_exp_f32_e32 v158, v64
	v_sub_f32_e32 v64, v79, v91
	s_waitcnt lgkmcnt(10)
	v_mfma_f32_16x16x32_bf16 v[88:91], v[184:187], v[4:7], v[92:95]
	ds_read_b64_tr_b16 v[176:177], v146 offset:40960
	ds_read_b64_tr_b16 v[184:185], v139 offset:32768
	ds_read_b64_tr_b16 v[186:187], v142 offset:32768
	v_exp_f32_e32 v159, v64
	v_mfma_f32_16x16x32_bf16 v[80:83], v[172:175], v[8:11], v[84:87]
	ds_read_b64_tr_b16 v[174:175], v142 offset:40960
	ds_read_b64_tr_b16 v[172:173], v139 offset:40960
	v_sub_f32_e32 v64, v72, v66
	v_sub_f32_e32 v70, v73, v67
	v_mfma_f32_16x16x32_bf16 v[76:79], v[188:191], v[8:11], v[88:91]
	v_sub_f32_e32 v68, v74, v68
	s_and_b64 vcc, exec, s[10:11]
	v_mfma_f32_16x16x32_bf16 v[92:95], v[192:195], v[0:3], v[240:243]
	v_mfma_f32_16x16x32_bf16 v[76:79], v[196:199], v[12:15], v[76:79]
	s_waitcnt lgkmcnt(11)
	v_mfma_f32_16x16x32_bf16 v[88:91], v[200:203], v[4:7], v[92:95]
	ds_read_b64_tr_b16 v[188:189], v141 offset:32768
	ds_read_b64_tr_b16 v[190:191], v145 offset:32768
	ds_read_b64_tr_b16 v[194:195], v145 offset:40960
	ds_read_b64_tr_b16 v[192:193], v141 offset:40960
	v_mfma_f32_16x16x32_bf16 v[80:83], v[180:183], v[12:15], v[80:83]
	v_exp_f32_e32 v160, v64
	v_exp_f32_e32 v161, v70
	v_mfma_f32_16x16x32_bf16 v[84:87], v[204:207], v[8:11], v[88:91]
	v_exp_f32_e32 v162, v68
	v_mfma_f32_16x16x32_bf16 v[64:67], v[212:215], v[12:15], v[84:87]
	v_sub_f32_e32 v68, v75, v69
	v_exp_f32_e32 v163, v68
	v_mfma_f32_16x16x32_bf16 v[84:87], v[208:211], v[0:3], v[240:243]
	v_cvt_pk_bf16_f32 v92, v96, v97
	v_cvt_pk_bf16_f32 v93, v98, v99
	s_waitcnt lgkmcnt(11)
	v_mfma_f32_16x16x32_bf16 v[84:87], v[216:219], v[4:7], v[84:87]
	ds_read_b64_tr_b16 v[196:197], v140 offset:32768
	ds_read_b64_tr_b16 v[198:199], v143 offset:32768
	ds_read_b64_tr_b16 v[202:203], v143 offset:40960
	ds_read_b64_tr_b16 v[200:201], v140 offset:40960
	v_cvt_pk_bf16_f32 v94, v152, v153
	v_cvt_pk_bf16_f32 v95, v154, v155
	v_mfma_f32_16x16x32_bf16 v[68:71], v[220:223], v[8:11], v[84:87]
	s_nop 2
	v_cvt_pk_bf16_f32 v84, v156, v157
	v_mfma_f32_16x16x32_bf16 v[68:71], v[164:167], v[12:15], v[68:71]
	v_cvt_pk_bf16_f32 v85, v158, v159
	v_cvt_pk_bf16_f32 v86, v160, v161
	s_waitcnt lgkmcnt(11)
	v_mfma_f32_16x16x32_bf16 v[60:63], v[168:171], v[92:95], v[60:63]
	ds_read_b64_tr_b16 v[180:181], v147 offset:32768
	ds_read_b64_tr_b16 v[182:183], v149 offset:32768
	ds_read_b64_tr_b16 v[206:207], v149 offset:40960
	ds_read_b64_tr_b16 v[204:205], v147 offset:40960
	v_cvt_pk_bf16_f32 v87, v162, v163
	s_nop 1
	v_mfma_f32_16x16x32_bf16 v[60:63], v[176:179], v[84:87], v[60:63]
	s_waitcnt lgkmcnt(11)
	v_mfma_f32_16x16x32_bf16 v[56:59], v[184:187], v[92:95], v[56:59]
	ds_read_b64_tr_b16 v[212:213], v133 offset:32768
	ds_read_b64_tr_b16 v[214:215], v134 offset:32768
	ds_read_b64_tr_b16 v[210:211], v134 offset:40960
	ds_read_b64_tr_b16 v[208:209], v133 offset:40960
	v_mfma_f32_16x16x32_bf16 v[56:59], v[172:175], v[84:87], v[56:59]
	s_waitcnt lgkmcnt(11)
	v_mfma_f32_16x16x32_bf16 v[52:55], v[188:191], v[92:95], v[52:55]
	ds_read_b64_tr_b16 v[216:217], v135 offset:32768
	ds_read_b64_tr_b16 v[218:219], v136 offset:32768
	ds_read_b64_tr_b16 v[222:223], v136 offset:40960
	ds_read_b64_tr_b16 v[220:221], v135 offset:40960
	v_mfma_f32_16x16x32_bf16 v[52:55], v[192:195], v[84:87], v[52:55]
	s_waitcnt lgkmcnt(11)
	v_mfma_f32_16x16x32_bf16 v[48:51], v[196:199], v[92:95], v[48:51]
	ds_read_b64_tr_b16 v[164:165], v137 offset:32768
	ds_read_b64_tr_b16 v[166:167], v138 offset:32768
	ds_read_b64_tr_b16 v[170:171], v138 offset:40960
	ds_read_b64_tr_b16 v[168:169], v137 offset:40960
	v_mfma_f32_16x16x32_bf16 v[48:51], v[200:203], v[84:87], v[48:51]
	s_waitcnt lgkmcnt(11)
	v_mfma_f32_16x16x32_bf16 v[32:35], v[180:183], v[92:95], v[32:35]
	v_mfma_f32_16x16x32_bf16 v[32:35], v[204:207], v[84:87], v[32:35]
	s_waitcnt lgkmcnt(7)
	v_mfma_f32_16x16x32_bf16 v[36:39], v[212:215], v[92:95], v[36:39]
	v_mfma_f32_16x16x32_bf16 v[36:39], v[208:211], v[84:87], v[36:39]
	s_waitcnt lgkmcnt(3)
	v_mfma_f32_16x16x32_bf16 v[40:43], v[216:219], v[92:95], v[40:43]
	v_mfma_f32_16x16x32_bf16 v[40:43], v[220:223], v[84:87], v[40:43]
	s_waitcnt lgkmcnt(0)
	v_mfma_f32_16x16x32_bf16 v[44:47], v[164:167], v[92:95], v[44:47]
	v_mfma_f32_16x16x32_bf16 v[44:47], v[168:171], v[84:87], v[44:47]
	s_cbranch_vccnz .LBB0_577
	v_add_u32_e32 v72, 0, v109
	s_waitcnt vmcnt(3)
	ds_write_b128 v100, v[16:19]
	s_waitcnt vmcnt(2)
	ds_write_b128 v124, v[20:23]
	s_waitcnt vmcnt(1)
	ds_write_b128 v72, v[24:27] offset:49152
	v_add_u32_e32 v72, 0, v112
	s_waitcnt vmcnt(0)
	ds_write_b128 v72, v[28:31] offset:49152

.LBB0_639:
	ds_read_b128 v[88:91], v128
	ds_read_b128 v[92:95], v128 offset:1024
	ds_read_b128 v[156:159], v129
	ds_read_b128 v[188:191], v129 offset:1024
	ds_read_b128 v[192:195], v130
	ds_read_b128 v[196:199], v130 offset:1024
	ds_read_b128 v[200:203], v131
	ds_read_b128 v[204:207], v131 offset:1024
	ds_read_b128 v[208:211], v128 offset:8192
	ds_read_b128 v[212:215], v128 offset:9216
	ds_read_b128 v[216:219], v129 offset:8192
	ds_read_b128 v[220:223], v129 offset:9216
	s_and_b64 vcc, exec, s[10:11]
	s_waitcnt lgkmcnt(8)
	v_mfma_f32_16x16x32_bf16 v[72:75], v[88:91], v[0:3], 0
	ds_read_b128 v[88:91], v130 offset:8192
	v_mfma_f32_16x16x32_bf16 v[80:83], v[92:95], v[0:3], 0
	ds_read_b128 v[92:95], v130 offset:9216
	v_mfma_f32_16x16x32_bf16 v[72:75], v[156:159], v[4:7], v[72:75]
	ds_read_b128 v[156:159], v131 offset:8192
	s_waitcnt lgkmcnt(7)
	v_mfma_f32_16x16x32_bf16 v[72:75], v[192:195], v[8:11], v[72:75]
	ds_read_b128 v[192:195], v131 offset:9216
	v_mfma_f32_16x16x32_bf16 v[76:79], v[200:203], v[12:15], v[72:75]
	ds_read_b64_tr_b16 v[200:201], v140 offset:49152
	ds_read_b64_tr_b16 v[202:203], v141 offset:49152
	v_mfma_f32_16x16x32_bf16 v[72:75], v[188:191], v[4:7], v[80:83]
	ds_read_b64_tr_b16 v[190:191], v141 offset:57344
	ds_read_b64_tr_b16 v[188:189], v140 offset:57344
	v_mfma_f32_16x16x32_bf16 v[72:75], v[196:199], v[8:11], v[72:75]
	ds_read_b64_tr_b16 v[196:197], v136 offset:49152
	ds_read_b64_tr_b16 v[198:199], v137 offset:49152
	v_mfma_f32_16x16x32_bf16 v[72:75], v[204:207], v[12:15], v[72:75]
	ds_read_b64_tr_b16 v[206:207], v137 offset:57344
	s_waitcnt lgkmcnt(11)
	v_mfma_f32_16x16x32_bf16 v[80:83], v[208:211], v[0:3], 0
	ds_read_b64_tr_b16 v[204:205], v136 offset:57344
	ds_read_b64_tr_b16 v[208:209], v138 offset:49152
	ds_read_b64_tr_b16 v[210:211], v142 offset:49152
	v_mfma_f32_16x16x32_bf16 v[80:83], v[216:219], v[4:7], v[80:83]
	ds_read_b64_tr_b16 v[218:219], v142 offset:57344
	s_waitcnt lgkmcnt(11)
	v_mfma_f32_16x16x32_bf16 v[80:83], v[88:91], v[8:11], v[80:83]
	ds_read_b64_tr_b16 v[216:217], v138 offset:57344
	ds_read_b64_tr_b16 v[88:89], v139 offset:49152
	ds_read_b64_tr_b16 v[90:91], v143 offset:49152
	v_mfma_f32_16x16x32_bf16 v[84:87], v[156:159], v[12:15], v[80:83]
	ds_read_b64_tr_b16 v[158:159], v143 offset:57344
	v_mfma_f32_16x16x32_bf16 v[80:83], v[212:215], v[0:3], 0
	v_mfma_f32_16x16x32_bf16 v[80:83], v[220:223], v[4:7], v[80:83]
	s_waitcnt lgkmcnt(10)
	v_mfma_f32_16x16x32_bf16 v[48:51], v[200:203], v[68:71], v[48:51]
	ds_read_b64_tr_b16 v[156:157], v139 offset:57344
	ds_read_b64_tr_b16 v[212:213], v145 offset:49152
	ds_read_b64_tr_b16 v[214:215], v146 offset:49152
	ds_read_b64_tr_b16 v[222:223], v146 offset:57344
	ds_read_b64_tr_b16 v[220:221], v145 offset:57344
	v_mfma_f32_16x16x32_bf16 v[48:51], v[188:191], v[64:67], v[48:51]
	s_waitcnt lgkmcnt(11)
	v_mfma_f32_16x16x32_bf16 v[40:43], v[196:199], v[68:71], v[40:43]
	ds_read_b64_tr_b16 v[200:201], v147 offset:49152
	ds_read_b64_tr_b16 v[202:203], v148 offset:49152
	ds_read_b64_tr_b16 v[190:191], v148 offset:57344
	ds_read_b64_tr_b16 v[188:189], v147 offset:57344
	v_mfma_f32_16x16x32_bf16 v[40:43], v[204:207], v[64:67], v[40:43]
	s_waitcnt lgkmcnt(11)
	v_mfma_f32_16x16x32_bf16 v[44:47], v[208:211], v[68:71], v[44:47]
	ds_read_b64_tr_b16 v[196:197], v149 offset:49152
	ds_read_b64_tr_b16 v[198:199], v150 offset:49152
	ds_read_b64_tr_b16 v[206:207], v150 offset:57344
	ds_read_b64_tr_b16 v[204:205], v149 offset:57344
	v_mfma_f32_16x16x32_bf16 v[44:47], v[216:219], v[64:67], v[44:47]
	s_waitcnt lgkmcnt(11)
	v_mfma_f32_16x16x32_bf16 v[56:59], v[88:91], v[68:71], v[56:59]
	ds_read_b64_tr_b16 v[208:209], v151 offset:49152
	ds_read_b64_tr_b16 v[210:211], v152 offset:49152
	ds_read_b64_tr_b16 v[218:219], v152 offset:57344
	ds_read_b64_tr_b16 v[216:217], v151 offset:57344
	v_mfma_f32_16x16x32_bf16 v[56:59], v[156:159], v[64:67], v[56:59]
	s_waitcnt lgkmcnt(11)
	v_mfma_f32_16x16x32_bf16 v[60:63], v[212:215], v[68:71], v[60:63]
	v_mfma_f32_16x16x32_bf16 v[60:63], v[220:223], v[64:67], v[60:63]
	s_waitcnt lgkmcnt(7)
	v_mfma_f32_16x16x32_bf16 v[52:55], v[200:203], v[68:71], v[52:55]
	v_mfma_f32_16x16x32_bf16 v[52:55], v[188:191], v[64:67], v[52:55]
	s_waitcnt lgkmcnt(3)
	v_mfma_f32_16x16x32_bf16 v[32:35], v[196:199], v[68:71], v[32:35]
	v_mfma_f32_16x16x32_bf16 v[32:35], v[204:207], v[64:67], v[32:35]
	v_mfma_f32_16x16x32_bf16 v[80:83], v[92:95], v[8:11], v[80:83]
	s_waitcnt lgkmcnt(0)
	v_mfma_f32_16x16x32_bf16 v[36:39], v[208:211], v[68:71], v[36:39]
	v_mfma_f32_16x16x32_bf16 v[80:83], v[192:195], v[12:15], v[80:83]
	v_mfma_f32_16x16x32_bf16 v[36:39], v[216:219], v[64:67], v[36:39]
	s_cbranch_vccnz .LBB0_641
	s_waitcnt vmcnt(3)
	ds_write_b128 v98, v[16:19] offset:16384
	s_waitcnt vmcnt(2)
	ds_write_b128 v99, v[20:23] offset:16384
	s_waitcnt vmcnt(1)
	ds_write_b128 v100, v[24:27] offset:32768
	s_waitcnt vmcnt(0)
	ds_write_b128 v124, v[28:31] offset:32768

.LBB0_663:
	ds_read_b128 v[176:179], v128 offset:16384
	ds_read_b128 v[180:183], v128 offset:17408
	ds_read_b128 v[188:191], v129 offset:16384
	ds_read_b128 v[192:195], v130 offset:16384
	ds_read_b128 v[196:199], v131 offset:16384
	ds_read_b128 v[200:203], v129 offset:17408
	ds_read_b128 v[204:207], v130 offset:17408
	ds_read_b128 v[208:211], v129 offset:24576
	ds_read_b128 v[212:215], v131 offset:17408
	ds_read_b128 v[216:219], v128 offset:24576
	ds_read_b128 v[220:223], v130 offset:24576
	v_pk_mul_f32 v[184:185], v[66:67], v[68:69]
	s_waitcnt lgkmcnt(7)
	v_mfma_f32_16x16x32_bf16 v[160:163], v[176:179], v[0:3], 0
	ds_read_b128 v[176:179], v128 offset:25600
	v_mul_f32_e32 v70, v70, v71
	v_mul_f32_e32 v157, v70, v157
	v_mul_f32_e32 v159, v157, v159
	v_mfma_f32_16x16x32_bf16 v[164:167], v[180:183], v[0:3], 0
	ds_read_b128 v[180:183], v131 offset:24576
	v_mul_f32_e32 v186, v153, v159
	v_pk_mul_f32 v[64:65], v[64:65], v[96:97]
	v_pk_mul_f32 v[72:73], v[72:73], v[74:75]
	v_mfma_f32_16x16x32_bf16 v[160:163], v[188:191], v[4:7], v[160:163]
	ds_read_b128 v[188:191], v129 offset:25600
	v_pk_mul_f32 v[96:97], v[64:65], v[186:187] op_sel_hi:[1,0]
	v_pk_mul_f32 v[84:85], v[84:85], v[94:95]
	v_mfma_f32_16x16x32_bf16 v[66:69], v[192:195], v[8:11], v[160:163]
	ds_read_b128 v[192:195], v130 offset:25600
	v_cvt_pk_bf16_f32 v173, v96, v97
	v_pk_mul_f32 v[96:97], v[76:77], v[78:79]
	s_waitcnt lgkmcnt(7)
	v_mfma_f32_16x16x32_bf16 v[68:71], v[196:199], v[12:15], v[66:69]
	ds_read_b128 v[196:199], v131 offset:25600
	v_pk_mul_f32 v[96:97], v[96:97], v[186:187] op_sel_hi:[1,0]
	v_pk_mul_f32 v[86:87], v[86:87], v[92:93]
	v_mfma_f32_16x16x32_bf16 v[164:167], v[200:203], v[4:7], v[164:167]
	ds_read_b64_tr_b16 v[200:201], v140 offset:32768
	ds_read_b64_tr_b16 v[202:203], v141 offset:32768
	v_mul_f32_e64 v66, v184, v186
	v_mul_f32_e64 v67, v185, v186
	v_pk_mul_f32 v[80:81], v[80:81], v[82:83]
	v_cvt_pk_bf16_f32 v172, v66, v67
	v_mfma_f32_16x16x32_bf16 v[64:67], v[204:207], v[8:11], v[164:167]
	ds_read_b64_tr_b16 v[206:207], v141 offset:40960
	ds_read_b64_tr_b16 v[204:205], v140 offset:40960
	s_and_b64 vcc, exec, s[10:11]
	s_waitcnt lgkmcnt(8)
	v_mfma_f32_16x16x32_bf16 v[64:67], v[212:215], v[12:15], v[64:67]
	ds_read_b64_tr_b16 v[212:213], v136 offset:32768
	ds_read_b64_tr_b16 v[214:215], v137 offset:32768
	v_mfma_f32_16x16x32_bf16 v[168:171], v[216:219], v[0:3], 0
	ds_read_b64_tr_b16 v[218:219], v137 offset:40960
	ds_read_b64_tr_b16 v[216:217], v136 offset:40960
	v_cvt_pk_bf16_f32 v174, v96, v97
	v_pk_mul_f32 v[96:97], v[72:73], v[186:187] op_sel_hi:[1,0]
	v_mfma_f32_16x16x32_bf16 v[76:79], v[208:211], v[4:7], v[168:171]
	ds_read_b64_tr_b16 v[208:209], v138 offset:32768
	ds_read_b64_tr_b16 v[210:211], v142 offset:32768
	v_cvt_pk_bf16_f32 v175, v96, v97
	v_mfma_f32_16x16x32_bf16 v[94:97], v[176:179], v[0:3], 0
	ds_read_b64_tr_b16 v[178:179], v142 offset:40960
	v_mfma_f32_16x16x32_bf16 v[72:75], v[220:223], v[8:11], v[76:79]
	v_mul_f32_e32 v162, v153, v158
	v_pk_mul_f32 v[84:85], v[84:85], v[162:163] op_sel_hi:[1,0]
	v_pk_mul_f32 v[86:87], v[86:87], v[162:163] op_sel_hi:[1,0]
	s_waitcnt lgkmcnt(10)
	v_mfma_f32_16x16x32_bf16 v[92:95], v[188:191], v[4:7], v[94:97]
	ds_read_b64_tr_b16 v[176:177], v138 offset:40960
	ds_read_b64_tr_b16 v[220:221], v139 offset:32768
	ds_read_b64_tr_b16 v[222:223], v143 offset:32768
	ds_read_b64_tr_b16 v[190:191], v143 offset:40960
	ds_read_b64_tr_b16 v[188:189], v139 offset:40960
	v_cvt_pk_bf16_f32 v84, v84, v85
	v_cvt_pk_bf16_f32 v85, v86, v87
	v_pk_mul_f32 v[86:87], v[88:89], v[90:91]
	v_mfma_f32_16x16x32_bf16 v[92:95], v[192:195], v[8:11], v[92:95]
	v_pk_mul_f32 v[86:87], v[86:87], v[162:163] op_sel_hi:[1,0]
	v_mfma_f32_16x16x32_bf16 v[76:79], v[196:199], v[12:15], v[92:95]
	v_cvt_pk_bf16_f32 v86, v86, v87
	s_nop 4
	v_pk_mul_f32 v[92:93], v[80:81], v[162:163] op_sel_hi:[1,0]
	s_waitcnt lgkmcnt(11)
	v_mfma_f32_16x16x32_bf16 v[48:51], v[200:203], v[172:175], v[48:51]
	ds_read_b64_tr_b16 v[192:193], v145 offset:32768
	ds_read_b64_tr_b16 v[194:195], v146 offset:32768
	ds_read_b64_tr_b16 v[198:199], v146 offset:40960
	ds_read_b64_tr_b16 v[196:197], v145 offset:40960
	v_cvt_pk_bf16_f32 v87, v92, v93
	s_waitcnt lgkmcnt(11)
	v_mfma_f32_16x16x32_bf16 v[40:43], v[212:215], v[172:175], v[40:43]
	ds_read_b64_tr_b16 v[200:201], v147 offset:32768
	ds_read_b64_tr_b16 v[202:203], v148 offset:32768
	ds_read_b64_tr_b16 v[214:215], v148 offset:40960
	ds_read_b64_tr_b16 v[212:213], v147 offset:40960
	v_mfma_f32_16x16x32_bf16 v[40:43], v[216:219], v[84:87], v[40:43]
	s_waitcnt lgkmcnt(11)
	v_mfma_f32_16x16x32_bf16 v[44:47], v[208:211], v[172:175], v[44:47]
	ds_read_b64_tr_b16 v[216:217], v149 offset:32768
	ds_read_b64_tr_b16 v[218:219], v150 offset:32768
	ds_read_b64_tr_b16 v[210:211], v150 offset:40960
	ds_read_b64_tr_b16 v[208:209], v149 offset:40960
	v_mfma_f32_16x16x32_bf16 v[44:47], v[176:179], v[84:87], v[44:47]
	s_waitcnt lgkmcnt(11)
	v_mfma_f32_16x16x32_bf16 v[56:59], v[220:223], v[172:175], v[56:59]
	ds_read_b64_tr_b16 v[176:177], v151 offset:32768
	ds_read_b64_tr_b16 v[178:179], v152 offset:32768
	ds_read_b64_tr_b16 v[222:223], v152 offset:40960
	ds_read_b64_tr_b16 v[220:221], v151 offset:40960
	v_mfma_f32_16x16x32_bf16 v[56:59], v[188:191], v[84:87], v[56:59]
	s_waitcnt lgkmcnt(11)
	v_mfma_f32_16x16x32_bf16 v[60:63], v[192:195], v[172:175], v[60:63]
	v_mfma_f32_16x16x32_bf16 v[60:63], v[196:199], v[84:87], v[60:63]
	s_waitcnt lgkmcnt(7)
	v_mfma_f32_16x16x32_bf16 v[52:55], v[200:203], v[172:175], v[52:55]
	v_mfma_f32_16x16x32_bf16 v[52:55], v[212:215], v[84:87], v[52:55]
	s_waitcnt lgkmcnt(3)
	v_mfma_f32_16x16x32_bf16 v[32:35], v[216:219], v[172:175], v[32:35]
	v_mfma_f32_16x16x32_bf16 v[32:35], v[208:211], v[84:87], v[32:35]
	s_waitcnt lgkmcnt(0)
	v_mfma_f32_16x16x32_bf16 v[36:39], v[176:179], v[172:175], v[36:39]
	v_mfma_f32_16x16x32_bf16 v[72:75], v[180:183], v[12:15], v[72:75]
	v_mfma_f32_16x16x32_bf16 v[48:51], v[204:207], v[84:87], v[48:51]
	v_mfma_f32_16x16x32_bf16 v[36:39], v[220:223], v[84:87], v[36:39]
	s_cbranch_vccnz .LBB0_665
	s_waitcnt vmcnt(3)
	ds_write_b128 v98, v[16:19]
	s_waitcnt vmcnt(2)
	ds_write_b128 v99, v[20:23]
	s_waitcnt vmcnt(1)
	ds_write_b128 v100, v[24:27] offset:49152
	s_waitcnt vmcnt(0)
	ds_write_b128 v124, v[28:31] offset:49152

.LBB0_742:
	ds_read_b128 v[88:91], v128
	ds_read_b128 v[92:95], v128 offset:1024
	ds_read_b128 v[156:159], v129
	ds_read_b128 v[188:191], v129 offset:1024
	ds_read_b128 v[192:195], v130
	ds_read_b128 v[196:199], v130 offset:1024
	ds_read_b128 v[200:203], v131
	ds_read_b128 v[204:207], v131 offset:1024
	ds_read_b128 v[208:211], v128 offset:8192
	ds_read_b128 v[212:215], v128 offset:9216
	ds_read_b128 v[216:219], v129 offset:8192
	ds_read_b128 v[220:223], v129 offset:9216
	s_and_b64 vcc, exec, s[10:11]
	s_waitcnt lgkmcnt(8)
	v_mfma_f32_16x16x32_bf16 v[72:75], v[88:91], v[0:3], 0
	ds_read_b128 v[88:91], v130 offset:8192
	v_mfma_f32_16x16x32_bf16 v[80:83], v[92:95], v[0:3], 0
	ds_read_b128 v[92:95], v130 offset:9216
	v_mfma_f32_16x16x32_bf16 v[72:75], v[156:159], v[4:7], v[72:75]
	ds_read_b128 v[156:159], v131 offset:8192
	s_waitcnt lgkmcnt(7)
	v_mfma_f32_16x16x32_bf16 v[72:75], v[192:195], v[8:11], v[72:75]
	ds_read_b128 v[192:195], v131 offset:9216
	v_mfma_f32_16x16x32_bf16 v[76:79], v[200:203], v[12:15], v[72:75]
	ds_read_b64_tr_b16 v[200:201], v142 offset:49152
	ds_read_b64_tr_b16 v[202:203], v143 offset:49152
	v_mfma_f32_16x16x32_bf16 v[72:75], v[188:191], v[4:7], v[80:83]
	ds_read_b64_tr_b16 v[190:191], v143 offset:57344
	ds_read_b64_tr_b16 v[188:189], v142 offset:57344
	v_mfma_f32_16x16x32_bf16 v[72:75], v[196:199], v[8:11], v[72:75]
	ds_read_b64_tr_b16 v[196:197], v136 offset:49152
	ds_read_b64_tr_b16 v[198:199], v139 offset:49152
	v_mfma_f32_16x16x32_bf16 v[72:75], v[204:207], v[12:15], v[72:75]
	ds_read_b64_tr_b16 v[206:207], v139 offset:57344
	s_waitcnt lgkmcnt(11)
	v_mfma_f32_16x16x32_bf16 v[80:83], v[208:211], v[0:3], 0
	ds_read_b64_tr_b16 v[204:205], v136 offset:57344
	ds_read_b64_tr_b16 v[208:209], v138 offset:49152
	ds_read_b64_tr_b16 v[210:211], v141 offset:49152
	v_mfma_f32_16x16x32_bf16 v[80:83], v[216:219], v[4:7], v[80:83]
	ds_read_b64_tr_b16 v[218:219], v141 offset:57344
	s_waitcnt lgkmcnt(11)
	v_mfma_f32_16x16x32_bf16 v[80:83], v[88:91], v[8:11], v[80:83]
	ds_read_b64_tr_b16 v[216:217], v138 offset:57344
	ds_read_b64_tr_b16 v[88:89], v137 offset:49152
	ds_read_b64_tr_b16 v[90:91], v140 offset:49152
	v_mfma_f32_16x16x32_bf16 v[84:87], v[156:159], v[12:15], v[80:83]
	ds_read_b64_tr_b16 v[158:159], v140 offset:57344
	v_mfma_f32_16x16x32_bf16 v[80:83], v[212:215], v[0:3], 0
	v_mfma_f32_16x16x32_bf16 v[80:83], v[220:223], v[4:7], v[80:83]
	s_waitcnt lgkmcnt(10)
	v_mfma_f32_16x16x32_bf16 v[60:63], v[200:203], v[64:67], v[60:63]
	ds_read_b64_tr_b16 v[156:157], v137 offset:57344
	ds_read_b64_tr_b16 v[212:213], v145 offset:49152
	ds_read_b64_tr_b16 v[214:215], v146 offset:49152
	ds_read_b64_tr_b16 v[222:223], v146 offset:57344
	ds_read_b64_tr_b16 v[220:221], v145 offset:57344
	v_mfma_f32_16x16x32_bf16 v[60:63], v[188:191], v[68:71], v[60:63]
	s_waitcnt lgkmcnt(11)
	v_mfma_f32_16x16x32_bf16 v[52:55], v[196:199], v[64:67], v[52:55]
	ds_read_b64_tr_b16 v[200:201], v147 offset:49152
	ds_read_b64_tr_b16 v[202:203], v148 offset:49152
	ds_read_b64_tr_b16 v[190:191], v148 offset:57344
	ds_read_b64_tr_b16 v[188:189], v147 offset:57344
	v_mfma_f32_16x16x32_bf16 v[52:55], v[204:207], v[68:71], v[52:55]
	s_waitcnt lgkmcnt(11)
	v_mfma_f32_16x16x32_bf16 v[44:47], v[208:211], v[64:67], v[44:47]
	ds_read_b64_tr_b16 v[196:197], v149 offset:49152
	ds_read_b64_tr_b16 v[198:199], v150 offset:49152
	ds_read_b64_tr_b16 v[206:207], v150 offset:57344
	ds_read_b64_tr_b16 v[204:205], v149 offset:57344
	v_mfma_f32_16x16x32_bf16 v[44:47], v[216:219], v[68:71], v[44:47]
	s_waitcnt lgkmcnt(11)
	v_mfma_f32_16x16x32_bf16 v[56:59], v[88:91], v[64:67], v[56:59]
	ds_read_b64_tr_b16 v[208:209], v151 offset:49152
	ds_read_b64_tr_b16 v[210:211], v152 offset:49152
	ds_read_b64_tr_b16 v[218:219], v152 offset:57344
	ds_read_b64_tr_b16 v[216:217], v151 offset:57344
	v_mfma_f32_16x16x32_bf16 v[56:59], v[156:159], v[68:71], v[56:59]
	s_waitcnt lgkmcnt(11)
	v_mfma_f32_16x16x32_bf16 v[48:51], v[212:215], v[64:67], v[48:51]
	v_mfma_f32_16x16x32_bf16 v[48:51], v[220:223], v[68:71], v[48:51]
	s_waitcnt lgkmcnt(7)
	v_mfma_f32_16x16x32_bf16 v[40:43], v[200:203], v[64:67], v[40:43]
	v_mfma_f32_16x16x32_bf16 v[40:43], v[188:191], v[68:71], v[40:43]
	s_waitcnt lgkmcnt(3)
	v_mfma_f32_16x16x32_bf16 v[32:35], v[196:199], v[64:67], v[32:35]
	v_mfma_f32_16x16x32_bf16 v[32:35], v[204:207], v[68:71], v[32:35]
	v_mfma_f32_16x16x32_bf16 v[80:83], v[92:95], v[8:11], v[80:83]
	s_waitcnt lgkmcnt(0)
	v_mfma_f32_16x16x32_bf16 v[36:39], v[208:211], v[64:67], v[36:39]
	v_mfma_f32_16x16x32_bf16 v[80:83], v[192:195], v[12:15], v[80:83]
	v_mfma_f32_16x16x32_bf16 v[36:39], v[216:219], v[68:71], v[36:39]
	s_cbranch_vccnz .LBB0_744
	s_waitcnt vmcnt(3)
	ds_write_b128 v98, v[16:19] offset:16384
	s_waitcnt vmcnt(2)
	ds_write_b128 v99, v[20:23] offset:16384
	s_waitcnt vmcnt(1)
	ds_write_b128 v100, v[24:27] offset:32768
	s_waitcnt vmcnt(0)
	ds_write_b128 v124, v[28:31] offset:32768

.LBB0_766:
	ds_read_b128 v[176:179], v128 offset:16384
	ds_read_b128 v[180:183], v128 offset:17408
	ds_read_b128 v[188:191], v129 offset:16384
	ds_read_b128 v[192:195], v130 offset:16384
	ds_read_b128 v[196:199], v131 offset:16384
	ds_read_b128 v[200:203], v129 offset:17408
	ds_read_b128 v[204:207], v130 offset:17408
	ds_read_b128 v[208:211], v129 offset:24576
	ds_read_b128 v[212:215], v131 offset:17408
	ds_read_b128 v[216:219], v128 offset:24576
	ds_read_b128 v[220:223], v130 offset:24576
	v_pk_mul_f32 v[184:185], v[66:67], v[68:69]
	s_waitcnt lgkmcnt(7)
	v_mfma_f32_16x16x32_bf16 v[160:163], v[176:179], v[0:3], 0
	ds_read_b128 v[176:179], v128 offset:25600
	v_mul_f32_e32 v70, v70, v71
	v_mul_f32_e32 v157, v70, v157
	v_mul_f32_e32 v159, v157, v159
	v_mfma_f32_16x16x32_bf16 v[164:167], v[180:183], v[0:3], 0
	ds_read_b128 v[180:183], v131 offset:24576
	v_mul_f32_e32 v186, v153, v159
	v_pk_mul_f32 v[64:65], v[64:65], v[96:97]
	v_pk_mul_f32 v[72:73], v[72:73], v[74:75]
	v_mfma_f32_16x16x32_bf16 v[160:163], v[188:191], v[4:7], v[160:163]
	ds_read_b128 v[188:191], v129 offset:25600
	v_pk_mul_f32 v[96:97], v[64:65], v[186:187] op_sel_hi:[1,0]
	v_pk_mul_f32 v[84:85], v[84:85], v[94:95]
	v_mfma_f32_16x16x32_bf16 v[66:69], v[192:195], v[8:11], v[160:163]
	ds_read_b128 v[192:195], v130 offset:25600
	v_cvt_pk_bf16_f32 v173, v96, v97
	v_pk_mul_f32 v[96:97], v[76:77], v[78:79]
	s_waitcnt lgkmcnt(7)
	v_mfma_f32_16x16x32_bf16 v[68:71], v[196:199], v[12:15], v[66:69]
	ds_read_b128 v[196:199], v131 offset:25600
	v_pk_mul_f32 v[96:97], v[96:97], v[186:187] op_sel_hi:[1,0]
	v_pk_mul_f32 v[86:87], v[86:87], v[92:93]
	v_mfma_f32_16x16x32_bf16 v[164:167], v[200:203], v[4:7], v[164:167]
	ds_read_b64_tr_b16 v[200:201], v142 offset:32768
	ds_read_b64_tr_b16 v[202:203], v143 offset:32768
	v_mul_f32_e64 v66, v184, v186
	v_mul_f32_e64 v67, v185, v186
	v_pk_mul_f32 v[80:81], v[80:81], v[82:83]
	v_cvt_pk_bf16_f32 v172, v66, v67
	v_mfma_f32_16x16x32_bf16 v[64:67], v[204:207], v[8:11], v[164:167]
	ds_read_b64_tr_b16 v[206:207], v143 offset:40960
	ds_read_b64_tr_b16 v[204:205], v142 offset:40960
	s_and_b64 vcc, exec, s[10:11]
	s_waitcnt lgkmcnt(8)
	v_mfma_f32_16x16x32_bf16 v[64:67], v[212:215], v[12:15], v[64:67]
	ds_read_b64_tr_b16 v[212:213], v136 offset:32768
	ds_read_b64_tr_b16 v[214:215], v139 offset:32768
	v_mfma_f32_16x16x32_bf16 v[168:171], v[216:219], v[0:3], 0
	ds_read_b64_tr_b16 v[218:219], v139 offset:40960
	ds_read_b64_tr_b16 v[216:217], v136 offset:40960
	v_cvt_pk_bf16_f32 v174, v96, v97
	v_pk_mul_f32 v[96:97], v[72:73], v[186:187] op_sel_hi:[1,0]
	v_mfma_f32_16x16x32_bf16 v[76:79], v[208:211], v[4:7], v[168:171]
	ds_read_b64_tr_b16 v[208:209], v138 offset:32768
	ds_read_b64_tr_b16 v[210:211], v141 offset:32768
	v_cvt_pk_bf16_f32 v175, v96, v97
	v_mfma_f32_16x16x32_bf16 v[94:97], v[176:179], v[0:3], 0
	ds_read_b64_tr_b16 v[178:179], v141 offset:40960
	v_mfma_f32_16x16x32_bf16 v[72:75], v[220:223], v[8:11], v[76:79]
	v_mul_f32_e32 v162, v153, v158
	v_pk_mul_f32 v[84:85], v[84:85], v[162:163] op_sel_hi:[1,0]
	v_pk_mul_f32 v[86:87], v[86:87], v[162:163] op_sel_hi:[1,0]
	s_waitcnt lgkmcnt(10)
	v_mfma_f32_16x16x32_bf16 v[92:95], v[188:191], v[4:7], v[94:97]
	ds_read_b64_tr_b16 v[176:177], v138 offset:40960
	ds_read_b64_tr_b16 v[220:221], v137 offset:32768
	ds_read_b64_tr_b16 v[222:223], v140 offset:32768
	ds_read_b64_tr_b16 v[190:191], v140 offset:40960
	ds_read_b64_tr_b16 v[188:189], v137 offset:40960
	v_cvt_pk_bf16_f32 v84, v84, v85
	v_cvt_pk_bf16_f32 v85, v86, v87
	v_pk_mul_f32 v[86:87], v[88:89], v[90:91]
	v_mfma_f32_16x16x32_bf16 v[92:95], v[192:195], v[8:11], v[92:95]
	v_pk_mul_f32 v[86:87], v[86:87], v[162:163] op_sel_hi:[1,0]
	v_mfma_f32_16x16x32_bf16 v[76:79], v[196:199], v[12:15], v[92:95]
	v_cvt_pk_bf16_f32 v86, v86, v87
	s_nop 4
	v_pk_mul_f32 v[92:93], v[80:81], v[162:163] op_sel_hi:[1,0]
	s_waitcnt lgkmcnt(11)
	v_mfma_f32_16x16x32_bf16 v[60:63], v[200:203], v[172:175], v[60:63]
	ds_read_b64_tr_b16 v[192:193], v145 offset:32768
	ds_read_b64_tr_b16 v[194:195], v146 offset:32768
	ds_read_b64_tr_b16 v[198:199], v146 offset:40960
	ds_read_b64_tr_b16 v[196:197], v145 offset:40960
	v_cvt_pk_bf16_f32 v87, v92, v93
	s_waitcnt lgkmcnt(11)
	v_mfma_f32_16x16x32_bf16 v[52:55], v[212:215], v[172:175], v[52:55]
	ds_read_b64_tr_b16 v[200:201], v147 offset:32768
	ds_read_b64_tr_b16 v[202:203], v148 offset:32768
	ds_read_b64_tr_b16 v[214:215], v148 offset:40960
	ds_read_b64_tr_b16 v[212:213], v147 offset:40960
	v_mfma_f32_16x16x32_bf16 v[52:55], v[216:219], v[84:87], v[52:55]
	s_waitcnt lgkmcnt(11)
	v_mfma_f32_16x16x32_bf16 v[44:47], v[208:211], v[172:175], v[44:47]
	ds_read_b64_tr_b16 v[216:217], v149 offset:32768
	ds_read_b64_tr_b16 v[218:219], v150 offset:32768
	ds_read_b64_tr_b16 v[210:211], v150 offset:40960
	ds_read_b64_tr_b16 v[208:209], v149 offset:40960
	v_mfma_f32_16x16x32_bf16 v[44:47], v[176:179], v[84:87], v[44:47]
	s_waitcnt lgkmcnt(11)
	v_mfma_f32_16x16x32_bf16 v[56:59], v[220:223], v[172:175], v[56:59]
	ds_read_b64_tr_b16 v[176:177], v151 offset:32768
	ds_read_b64_tr_b16 v[178:179], v152 offset:32768
	ds_read_b64_tr_b16 v[222:223], v152 offset:40960
	ds_read_b64_tr_b16 v[220:221], v151 offset:40960
	v_mfma_f32_16x16x32_bf16 v[56:59], v[188:191], v[84:87], v[56:59]
	s_waitcnt lgkmcnt(11)
	v_mfma_f32_16x16x32_bf16 v[48:51], v[192:195], v[172:175], v[48:51]
	v_mfma_f32_16x16x32_bf16 v[48:51], v[196:199], v[84:87], v[48:51]
	s_waitcnt lgkmcnt(7)
	v_mfma_f32_16x16x32_bf16 v[40:43], v[200:203], v[172:175], v[40:43]
	v_mfma_f32_16x16x32_bf16 v[40:43], v[212:215], v[84:87], v[40:43]
	s_waitcnt lgkmcnt(3)
	v_mfma_f32_16x16x32_bf16 v[32:35], v[216:219], v[172:175], v[32:35]
	v_mfma_f32_16x16x32_bf16 v[32:35], v[208:211], v[84:87], v[32:35]
	s_waitcnt lgkmcnt(0)
	v_mfma_f32_16x16x32_bf16 v[36:39], v[176:179], v[172:175], v[36:39]
	v_mfma_f32_16x16x32_bf16 v[72:75], v[180:183], v[12:15], v[72:75]
	v_mfma_f32_16x16x32_bf16 v[60:63], v[204:207], v[84:87], v[60:63]
	v_mfma_f32_16x16x32_bf16 v[36:39], v[220:223], v[84:87], v[36:39]
	s_cbranch_vccnz .LBB0_768
	s_waitcnt vmcnt(3)
	ds_write_b128 v98, v[16:19]
	s_waitcnt vmcnt(2)
	ds_write_b128 v99, v[20:23]
	s_waitcnt vmcnt(1)
	ds_write_b128 v100, v[24:27] offset:49152
	s_waitcnt vmcnt(0)
	ds_write_b128 v124, v[28:31] offset:49152

.LBB0_1919:
	ds_read_b128 v[88:91], v129
	ds_read_b128 v[92:95], v129 offset:1024
	ds_read_b128 v[96:99], v130
	ds_read_b128 v[152:155], v130 offset:1024
	ds_read_b128 v[176:179], v131
	ds_read_b128 v[180:183], v131 offset:1024
	ds_read_b128 v[184:187], v132
	ds_read_b128 v[188:191], v132 offset:1024
	ds_read_b128 v[192:195], v129 offset:8192
	ds_read_b128 v[196:199], v129 offset:9216
	ds_read_b128 v[200:203], v130 offset:8192
	ds_read_b128 v[204:207], v130 offset:9216
	ds_read_b128 v[208:211], v131 offset:8192
	ds_read_b128 v[212:215], v131 offset:9216
	ds_read_b128 v[216:219], v132 offset:8192
	s_and_b64 vcc, exec, s[6:7]
	s_waitcnt lgkmcnt(11)
	v_mfma_f32_16x16x32_bf16 v[72:75], v[88:91], v[0:3], v[240:243]
	ds_read_b128 v[220:223], v132 offset:9216
	ds_read_b64_tr_b16 v[88:89], v142 offset:49152
	ds_read_b64_tr_b16 v[90:91], v146 offset:49152
	v_mfma_f32_16x16x32_bf16 v[72:75], v[96:99], v[4:7], v[72:75]
	ds_read_b64_tr_b16 v[98:99], v146 offset:57344
	v_mfma_f32_16x16x32_bf16 v[76:79], v[92:95], v[0:3], v[240:243]
	s_waitcnt lgkmcnt(11)
	v_mfma_f32_16x16x32_bf16 v[72:75], v[176:179], v[8:11], v[72:75]
	ds_read_b64_tr_b16 v[96:97], v142 offset:57344
	ds_read_b64_tr_b16 v[92:93], v136 offset:49152
	ds_read_b64_tr_b16 v[94:95], v137 offset:49152
	ds_read_b64_tr_b16 v[178:179], v137 offset:57344
	v_mfma_f32_16x16x32_bf16 v[84:87], v[184:187], v[12:15], v[72:75]
	v_mfma_f32_16x16x32_bf16 v[72:75], v[152:155], v[4:7], v[76:79]
	v_mfma_f32_16x16x32_bf16 v[72:75], v[180:183], v[8:11], v[72:75]
	v_mfma_f32_16x16x32_bf16 v[80:83], v[188:191], v[12:15], v[72:75]
	s_waitcnt lgkmcnt(11)
	s_nop 5
	v_mfma_f32_16x16x32_bf16 v[72:75], v[192:195], v[0:3], v[240:243]
	ds_read_b64_tr_b16 v[176:177], v136 offset:57344
	ds_read_b64_tr_b16 v[184:185], v139 offset:49152
	ds_read_b64_tr_b16 v[186:187], v145 offset:49152
	ds_read_b64_tr_b16 v[154:155], v145 offset:57344
	v_mfma_f32_16x16x32_bf16 v[72:75], v[200:203], v[4:7], v[72:75]
	s_waitcnt lgkmcnt(11)
	v_mfma_f32_16x16x32_bf16 v[72:75], v[208:211], v[8:11], v[72:75]
	ds_read_b64_tr_b16 v[152:153], v139 offset:57344
	ds_read_b64_tr_b16 v[180:181], v140 offset:49152
	ds_read_b64_tr_b16 v[182:183], v147 offset:49152
	ds_read_b64_tr_b16 v[190:191], v147 offset:57344
	v_mfma_f32_16x16x32_bf16 v[76:79], v[216:219], v[12:15], v[72:75]
	v_mfma_f32_16x16x32_bf16 v[72:75], v[196:199], v[0:3], v[240:243]
	v_mfma_f32_16x16x32_bf16 v[72:75], v[204:207], v[4:7], v[72:75]
	s_waitcnt lgkmcnt(10)
	v_mfma_f32_16x16x32_bf16 v[60:63], v[88:91], v[68:71], v[60:63]
	ds_read_b64_tr_b16 v[188:189], v140 offset:57344
	ds_read_b64_tr_b16 v[192:193], v148 offset:49152
	ds_read_b64_tr_b16 v[194:195], v149 offset:49152
	ds_read_b64_tr_b16 v[202:203], v149 offset:57344
	ds_read_b64_tr_b16 v[200:201], v148 offset:57344
	v_mfma_f32_16x16x32_bf16 v[60:63], v[96:99], v[64:67], v[60:63]
	s_waitcnt lgkmcnt(11)
	v_mfma_f32_16x16x32_bf16 v[52:55], v[92:95], v[68:71], v[52:55]
	ds_read_b64_tr_b16 v[208:209], v133 offset:49152
	ds_read_b64_tr_b16 v[210:211], v134 offset:49152
	ds_read_b64_tr_b16 v[218:219], v134 offset:57344
	ds_read_b64_tr_b16 v[216:217], v133 offset:57344
	v_mfma_f32_16x16x32_bf16 v[52:55], v[176:179], v[64:67], v[52:55]
	s_waitcnt lgkmcnt(11)
	v_mfma_f32_16x16x32_bf16 v[48:51], v[184:187], v[68:71], v[48:51]
	ds_read_b64_tr_b16 v[196:197], v135 offset:49152
	ds_read_b64_tr_b16 v[198:199], v138 offset:49152
	ds_read_b64_tr_b16 v[206:207], v138 offset:57344
	ds_read_b64_tr_b16 v[204:205], v135 offset:57344
	v_mfma_f32_16x16x32_bf16 v[48:51], v[152:155], v[64:67], v[48:51]
	s_waitcnt lgkmcnt(11)
	v_mfma_f32_16x16x32_bf16 v[56:59], v[180:183], v[68:71], v[56:59]
	ds_read_b64_tr_b16 v[88:89], v141 offset:49152
	ds_read_b64_tr_b16 v[90:91], v143 offset:49152
	ds_read_b64_tr_b16 v[98:99], v143 offset:57344
	ds_read_b64_tr_b16 v[96:97], v141 offset:57344
	v_mfma_f32_16x16x32_bf16 v[56:59], v[188:191], v[64:67], v[56:59]
	s_waitcnt lgkmcnt(11)
	v_mfma_f32_16x16x32_bf16 v[32:35], v[192:195], v[68:71], v[32:35]
	v_mfma_f32_16x16x32_bf16 v[32:35], v[200:203], v[64:67], v[32:35]
	s_waitcnt lgkmcnt(7)
	v_mfma_f32_16x16x32_bf16 v[36:39], v[208:211], v[68:71], v[36:39]
	v_mfma_f32_16x16x32_bf16 v[36:39], v[216:219], v[64:67], v[36:39]
	s_waitcnt lgkmcnt(3)
	v_mfma_f32_16x16x32_bf16 v[40:43], v[196:199], v[68:71], v[40:43]
	v_mfma_f32_16x16x32_bf16 v[40:43], v[204:207], v[64:67], v[40:43]
	v_mfma_f32_16x16x32_bf16 v[72:75], v[212:215], v[8:11], v[72:75]
	s_waitcnt lgkmcnt(0)
	v_mfma_f32_16x16x32_bf16 v[44:47], v[88:91], v[68:71], v[44:47]
	v_mfma_f32_16x16x32_bf16 v[72:75], v[220:223], v[12:15], v[72:75]
	v_mfma_f32_16x16x32_bf16 v[44:47], v[96:99], v[64:67], v[44:47]
	s_cbranch_vccnz .LBB0_1921
	v_add_u32_e32 v64, 0, v109
	s_waitcnt vmcnt(3)
	ds_write_b128 v100, v[16:19] offset:16384
	s_waitcnt vmcnt(2)
	ds_write_b128 v124, v[20:23] offset:16384
	s_waitcnt vmcnt(1)
	ds_write_b128 v64, v[24:27] offset:32768
	v_add_u32_e32 v64, 0, v112
	s_waitcnt vmcnt(0)
	ds_write_b128 v64, v[28:31] offset:32768

.LBB0_1927:
	ds_read_b128 v[168:171], v129 offset:16384
	ds_read_b128 v[172:175], v130 offset:16384
	ds_read_b128 v[176:179], v131 offset:16384
	ds_read_b128 v[180:183], v129 offset:17408
	ds_read_b128 v[184:187], v132 offset:16384
	ds_read_b128 v[188:191], v130 offset:17408
	ds_read_b128 v[192:195], v131 offset:17408
	ds_read_b128 v[196:199], v129 offset:24576
	ds_read_b128 v[200:203], v132 offset:17408
	ds_read_b128 v[204:207], v130 offset:24576
	ds_read_b128 v[208:211], v131 offset:24576
	ds_read_b128 v[212:215], v129 offset:25600
	ds_read_b128 v[216:219], v132 offset:24576
	ds_read_b128 v[220:223], v130 offset:25600
	v_sub_f32_e32 v64, v84, v96
	v_exp_f32_e32 v96, v64
	v_sub_f32_e32 v64, v85, v97
	v_exp_f32_e32 v97, v64
	v_sub_f32_e32 v64, v86, v98
	v_exp_f32_e32 v98, v64
	v_sub_f32_e32 v64, v87, v99
	v_exp_f32_e32 v99, v64
	v_sub_f32_e32 v64, v80, v92
	v_exp_f32_e32 v153, v64
	v_sub_f32_e32 v64, v81, v93
	v_exp_f32_e32 v154, v64
	v_sub_f32_e32 v64, v82, v94
	v_exp_f32_e32 v155, v64
	v_sub_f32_e32 v64, v83, v95
	s_waitcnt lgkmcnt(10)
	v_mfma_f32_16x16x32_bf16 v[84:87], v[168:171], v[0:3], v[240:243]
	ds_read_b128 v[168:171], v131 offset:25600
	v_exp_f32_e32 v156, v64
	v_sub_f32_e32 v64, v76, v88
	v_exp_f32_e32 v157, v64
	v_mfma_f32_16x16x32_bf16 v[92:95], v[180:183], v[0:3], v[240:243]
	ds_read_b128 v[180:183], v132 offset:25600
	v_sub_f32_e32 v64, v77, v89
	v_sub_f32_e32 v70, v73, v67
	v_mfma_f32_16x16x32_bf16 v[84:87], v[172:175], v[4:7], v[84:87]
	ds_read_b64_tr_b16 v[172:173], v142 offset:32768
	ds_read_b64_tr_b16 v[174:175], v146 offset:32768
	v_exp_f32_e32 v158, v64
	v_sub_f32_e32 v64, v78, v90
	v_exp_f32_e32 v159, v64
	v_sub_f32_e32 v64, v79, v91
	s_waitcnt lgkmcnt(9)
	v_mfma_f32_16x16x32_bf16 v[88:91], v[188:191], v[4:7], v[92:95]
	ds_read_b64_tr_b16 v[190:191], v146 offset:40960
	ds_read_b64_tr_b16 v[188:189], v142 offset:40960
	v_exp_f32_e32 v160, v64
	v_mfma_f32_16x16x32_bf16 v[80:83], v[176:179], v[8:11], v[84:87]
	ds_read_b64_tr_b16 v[176:177], v136 offset:32768
	ds_read_b64_tr_b16 v[178:179], v137 offset:32768
	v_sub_f32_e32 v64, v72, v66
	v_exp_f32_e32 v161, v64
	v_mfma_f32_16x16x32_bf16 v[76:79], v[192:195], v[8:11], v[88:91]
	ds_read_b64_tr_b16 v[194:195], v137 offset:40960
	ds_read_b64_tr_b16 v[192:193], v136 offset:40960
	v_sub_f32_e32 v68, v74, v68
	s_and_b64 vcc, exec, s[6:7]
	v_mfma_f32_16x16x32_bf16 v[92:95], v[196:199], v[0:3], v[240:243]
	v_mfma_f32_16x16x32_bf16 v[80:83], v[184:187], v[12:15], v[80:83]
	v_exp_f32_e32 v162, v70
	v_exp_f32_e32 v163, v68
	v_mfma_f32_16x16x32_bf16 v[76:79], v[200:203], v[12:15], v[76:79]
	s_waitcnt lgkmcnt(11)
	v_mfma_f32_16x16x32_bf16 v[88:91], v[204:207], v[4:7], v[92:95]
	ds_read_b64_tr_b16 v[196:197], v139 offset:32768
	ds_read_b64_tr_b16 v[198:199], v145 offset:32768
	ds_read_b64_tr_b16 v[186:187], v145 offset:40960
	ds_read_b64_tr_b16 v[184:185], v139 offset:40960
	v_sub_f32_e32 v68, v75, v69
	v_mfma_f32_16x16x32_bf16 v[84:87], v[208:211], v[8:11], v[88:91]
	v_cvt_pk_bf16_f32 v92, v96, v97
	v_cvt_pk_bf16_f32 v93, v98, v99
	v_cvt_pk_bf16_f32 v94, v153, v154
	v_mfma_f32_16x16x32_bf16 v[64:67], v[216:219], v[12:15], v[84:87]
	v_cvt_pk_bf16_f32 v95, v155, v156
	v_mfma_f32_16x16x32_bf16 v[84:87], v[212:215], v[0:3], v[240:243]
	v_exp_f32_e32 v164, v68
	s_waitcnt lgkmcnt(11)
	v_mfma_f32_16x16x32_bf16 v[84:87], v[220:223], v[4:7], v[84:87]
	ds_read_b64_tr_b16 v[200:201], v140 offset:32768
	ds_read_b64_tr_b16 v[202:203], v147 offset:32768
	ds_read_b64_tr_b16 v[206:207], v147 offset:40960
	ds_read_b64_tr_b16 v[204:205], v140 offset:40960
	v_mfma_f32_16x16x32_bf16 v[68:71], v[168:171], v[8:11], v[84:87]
	s_nop 2
	v_cvt_pk_bf16_f32 v84, v157, v158
	v_mfma_f32_16x16x32_bf16 v[68:71], v[180:183], v[12:15], v[68:71]
	v_cvt_pk_bf16_f32 v85, v159, v160
	v_cvt_pk_bf16_f32 v86, v161, v162
	s_waitcnt lgkmcnt(11)
	v_mfma_f32_16x16x32_bf16 v[60:63], v[172:175], v[92:95], v[60:63]
	ds_read_b64_tr_b16 v[208:209], v148 offset:32768
	ds_read_b64_tr_b16 v[210:211], v149 offset:32768
	ds_read_b64_tr_b16 v[218:219], v149 offset:40960
	ds_read_b64_tr_b16 v[216:217], v148 offset:40960
	v_cvt_pk_bf16_f32 v87, v163, v164
	s_nop 1
	v_mfma_f32_16x16x32_bf16 v[60:63], v[188:191], v[84:87], v[60:63]
	s_waitcnt lgkmcnt(11)
	v_mfma_f32_16x16x32_bf16 v[52:55], v[176:179], v[92:95], v[52:55]
	ds_read_b64_tr_b16 v[212:213], v133 offset:32768
	ds_read_b64_tr_b16 v[214:215], v134 offset:32768
	ds_read_b64_tr_b16 v[222:223], v134 offset:40960
	ds_read_b64_tr_b16 v[220:221], v133 offset:40960
	v_mfma_f32_16x16x32_bf16 v[52:55], v[192:195], v[84:87], v[52:55]
	s_waitcnt lgkmcnt(11)
	v_mfma_f32_16x16x32_bf16 v[48:51], v[196:199], v[92:95], v[48:51]
	ds_read_b64_tr_b16 v[168:169], v135 offset:32768
	ds_read_b64_tr_b16 v[170:171], v138 offset:32768
	ds_read_b64_tr_b16 v[182:183], v138 offset:40960
	ds_read_b64_tr_b16 v[180:181], v135 offset:40960
	v_mfma_f32_16x16x32_bf16 v[48:51], v[184:187], v[84:87], v[48:51]
	s_waitcnt lgkmcnt(11)
	v_mfma_f32_16x16x32_bf16 v[56:59], v[200:203], v[92:95], v[56:59]
	ds_read_b64_tr_b16 v[172:173], v141 offset:32768
	ds_read_b64_tr_b16 v[174:175], v143 offset:32768
	ds_read_b64_tr_b16 v[190:191], v143 offset:40960
	ds_read_b64_tr_b16 v[188:189], v141 offset:40960
	v_mfma_f32_16x16x32_bf16 v[56:59], v[204:207], v[84:87], v[56:59]
	s_waitcnt lgkmcnt(11)
	v_mfma_f32_16x16x32_bf16 v[32:35], v[208:211], v[92:95], v[32:35]
	v_mfma_f32_16x16x32_bf16 v[32:35], v[216:219], v[84:87], v[32:35]
	s_waitcnt lgkmcnt(7)
	v_mfma_f32_16x16x32_bf16 v[36:39], v[212:215], v[92:95], v[36:39]
	v_mfma_f32_16x16x32_bf16 v[36:39], v[220:223], v[84:87], v[36:39]
	s_waitcnt lgkmcnt(3)
	v_mfma_f32_16x16x32_bf16 v[40:43], v[168:171], v[92:95], v[40:43]
	v_mfma_f32_16x16x32_bf16 v[40:43], v[180:183], v[84:87], v[40:43]
	s_waitcnt lgkmcnt(0)
	v_mfma_f32_16x16x32_bf16 v[44:47], v[172:175], v[92:95], v[44:47]
	v_mfma_f32_16x16x32_bf16 v[44:47], v[188:191], v[84:87], v[44:47]
	s_cbranch_vccnz .LBB0_1929
	v_add_u32_e32 v72, 0, v109
	s_waitcnt vmcnt(3)
	ds_write_b128 v100, v[16:19]
	s_waitcnt vmcnt(2)
	ds_write_b128 v124, v[20:23]
	s_waitcnt vmcnt(1)
	ds_write_b128 v72, v[24:27] offset:49152
	v_add_u32_e32 v72, 0, v112
	s_waitcnt vmcnt(0)
	ds_write_b128 v72, v[28:31] offset:49152

.LBB0_1958:
	ds_read_b128 v[88:91], v129
	ds_read_b128 v[92:95], v129 offset:1024
	ds_read_b128 v[96:99], v130
	ds_read_b128 v[152:155], v130 offset:1024
	ds_read_b128 v[172:175], v131
	ds_read_b128 v[176:179], v131 offset:1024
	ds_read_b128 v[180:183], v132
	ds_read_b128 v[184:187], v132 offset:1024
	ds_read_b128 v[188:191], v129 offset:8192
	ds_read_b128 v[192:195], v129 offset:9216
	ds_read_b128 v[196:199], v130 offset:8192
	ds_read_b128 v[200:203], v130 offset:9216
	ds_read_b128 v[204:207], v131 offset:8192
	ds_read_b128 v[208:211], v131 offset:9216
	ds_read_b128 v[212:215], v132 offset:8192
	s_and_b64 vcc, exec, s[6:7]
	s_waitcnt lgkmcnt(11)
	v_mfma_f32_16x16x32_bf16 v[72:75], v[88:91], v[0:3], v[240:243]
	ds_read_b128 v[216:219], v132 offset:9216
	ds_read_b64_tr_b16 v[220:221], v146 offset:49152
	ds_read_b64_tr_b16 v[222:223], v148 offset:49152
	ds_read_b64_tr_b16 v[90:91], v148 offset:57344
	v_mfma_f32_16x16x32_bf16 v[72:75], v[96:99], v[4:7], v[72:75]
	v_mfma_f32_16x16x32_bf16 v[76:79], v[92:95], v[0:3], v[240:243]
	s_waitcnt lgkmcnt(11)
	v_mfma_f32_16x16x32_bf16 v[72:75], v[172:175], v[8:11], v[72:75]
	ds_read_b64_tr_b16 v[88:89], v146 offset:57344
	ds_read_b64_tr_b16 v[96:97], v139 offset:49152
	ds_read_b64_tr_b16 v[98:99], v142 offset:49152
	ds_read_b64_tr_b16 v[94:95], v142 offset:57344
	v_mfma_f32_16x16x32_bf16 v[84:87], v[180:183], v[12:15], v[72:75]
	v_mfma_f32_16x16x32_bf16 v[72:75], v[152:155], v[4:7], v[76:79]
	v_mfma_f32_16x16x32_bf16 v[72:75], v[176:179], v[8:11], v[72:75]
	v_mfma_f32_16x16x32_bf16 v[80:83], v[184:187], v[12:15], v[72:75]
	s_waitcnt lgkmcnt(11)
	s_nop 5
	v_mfma_f32_16x16x32_bf16 v[72:75], v[188:191], v[0:3], v[240:243]
	ds_read_b64_tr_b16 v[92:93], v139 offset:57344
	ds_read_b64_tr_b16 v[172:173], v141 offset:49152
	ds_read_b64_tr_b16 v[174:175], v145 offset:49152
	ds_read_b64_tr_b16 v[182:183], v145 offset:57344
	v_mfma_f32_16x16x32_bf16 v[72:75], v[196:199], v[4:7], v[72:75]
	s_waitcnt lgkmcnt(11)
	v_mfma_f32_16x16x32_bf16 v[72:75], v[204:207], v[8:11], v[72:75]
	ds_read_b64_tr_b16 v[180:181], v141 offset:57344
	ds_read_b64_tr_b16 v[152:153], v140 offset:49152
	ds_read_b64_tr_b16 v[154:155], v143 offset:49152
	ds_read_b64_tr_b16 v[178:179], v143 offset:57344
	v_mfma_f32_16x16x32_bf16 v[76:79], v[212:215], v[12:15], v[72:75]
	v_mfma_f32_16x16x32_bf16 v[72:75], v[192:195], v[0:3], v[240:243]
	v_mfma_f32_16x16x32_bf16 v[72:75], v[200:203], v[4:7], v[72:75]
	s_waitcnt lgkmcnt(10)
	v_mfma_f32_16x16x32_bf16 v[60:63], v[220:223], v[68:71], v[60:63]
	ds_read_b64_tr_b16 v[176:177], v140 offset:57344
	ds_read_b64_tr_b16 v[184:185], v147 offset:49152
	ds_read_b64_tr_b16 v[186:187], v149 offset:49152
	ds_read_b64_tr_b16 v[190:191], v149 offset:57344
	ds_read_b64_tr_b16 v[188:189], v147 offset:57344
	v_mfma_f32_16x16x32_bf16 v[60:63], v[88:91], v[64:67], v[60:63]
	s_waitcnt lgkmcnt(11)
	v_mfma_f32_16x16x32_bf16 v[56:59], v[96:99], v[68:71], v[56:59]
	ds_read_b64_tr_b16 v[196:197], v133 offset:49152
	ds_read_b64_tr_b16 v[198:199], v134 offset:49152
	ds_read_b64_tr_b16 v[206:207], v134 offset:57344
	ds_read_b64_tr_b16 v[204:205], v133 offset:57344
	v_mfma_f32_16x16x32_bf16 v[56:59], v[92:95], v[64:67], v[56:59]
	s_waitcnt lgkmcnt(11)
	v_mfma_f32_16x16x32_bf16 v[52:55], v[172:175], v[68:71], v[52:55]
	ds_read_b64_tr_b16 v[212:213], v135 offset:49152
	ds_read_b64_tr_b16 v[214:215], v136 offset:49152
	ds_read_b64_tr_b16 v[194:195], v136 offset:57344
	ds_read_b64_tr_b16 v[192:193], v135 offset:57344
	v_mfma_f32_16x16x32_bf16 v[52:55], v[180:183], v[64:67], v[52:55]
	s_waitcnt lgkmcnt(11)
	v_mfma_f32_16x16x32_bf16 v[48:51], v[152:155], v[68:71], v[48:51]
	ds_read_b64_tr_b16 v[200:201], v137 offset:49152
	ds_read_b64_tr_b16 v[202:203], v138 offset:49152
	ds_read_b64_tr_b16 v[222:223], v138 offset:57344
	ds_read_b64_tr_b16 v[220:221], v137 offset:57344
	v_mfma_f32_16x16x32_bf16 v[48:51], v[176:179], v[64:67], v[48:51]
	s_waitcnt lgkmcnt(11)
	v_mfma_f32_16x16x32_bf16 v[32:35], v[184:187], v[68:71], v[32:35]
	v_mfma_f32_16x16x32_bf16 v[32:35], v[188:191], v[64:67], v[32:35]
	s_waitcnt lgkmcnt(7)
	v_mfma_f32_16x16x32_bf16 v[36:39], v[196:199], v[68:71], v[36:39]
	v_mfma_f32_16x16x32_bf16 v[36:39], v[204:207], v[64:67], v[36:39]
	s_waitcnt lgkmcnt(3)
	v_mfma_f32_16x16x32_bf16 v[40:43], v[212:215], v[68:71], v[40:43]
	v_mfma_f32_16x16x32_bf16 v[40:43], v[192:195], v[64:67], v[40:43]
	v_mfma_f32_16x16x32_bf16 v[72:75], v[208:211], v[8:11], v[72:75]
	s_waitcnt lgkmcnt(0)
	v_mfma_f32_16x16x32_bf16 v[44:47], v[200:203], v[68:71], v[44:47]
	v_mfma_f32_16x16x32_bf16 v[72:75], v[216:219], v[12:15], v[72:75]
	v_mfma_f32_16x16x32_bf16 v[44:47], v[220:223], v[64:67], v[44:47]
	s_cbranch_vccnz .LBB0_1960
	v_add_u32_e32 v64, 0, v109
	s_waitcnt vmcnt(3)
	ds_write_b128 v100, v[16:19] offset:16384
	s_waitcnt vmcnt(2)
	ds_write_b128 v124, v[20:23] offset:16384
	s_waitcnt vmcnt(1)
	ds_write_b128 v64, v[24:27] offset:32768
	v_add_u32_e32 v64, 0, v112
	s_waitcnt vmcnt(0)
	ds_write_b128 v64, v[28:31] offset:32768

.LBB0_1966:
	ds_read_b128 v[164:167], v129 offset:16384
	ds_read_b128 v[168:171], v130 offset:16384
	ds_read_b128 v[172:175], v131 offset:16384
	ds_read_b128 v[176:179], v129 offset:17408
	ds_read_b128 v[180:183], v132 offset:16384
	ds_read_b128 v[184:187], v130 offset:17408
	ds_read_b128 v[188:191], v131 offset:17408
	ds_read_b128 v[192:195], v129 offset:24576
	ds_read_b128 v[196:199], v132 offset:17408
	ds_read_b128 v[200:203], v130 offset:24576
	ds_read_b128 v[204:207], v131 offset:24576
	ds_read_b128 v[208:211], v129 offset:25600
	ds_read_b128 v[212:215], v132 offset:24576
	ds_read_b128 v[216:219], v130 offset:25600
	ds_read_b128 v[220:223], v131 offset:25600
	v_sub_f32_e32 v64, v84, v96
	v_exp_f32_e32 v96, v64
	v_sub_f32_e32 v64, v85, v97
	v_exp_f32_e32 v97, v64
	v_sub_f32_e32 v64, v86, v98
	v_exp_f32_e32 v98, v64
	v_sub_f32_e32 v64, v87, v99
	v_exp_f32_e32 v99, v64
	v_sub_f32_e32 v64, v80, v92
	v_exp_f32_e32 v152, v64
	v_sub_f32_e32 v64, v81, v93
	v_exp_f32_e32 v153, v64
	v_sub_f32_e32 v64, v82, v94
	v_exp_f32_e32 v154, v64
	v_sub_f32_e32 v64, v83, v95
	s_waitcnt lgkmcnt(11)
	v_mfma_f32_16x16x32_bf16 v[84:87], v[164:167], v[0:3], v[240:243]
	ds_read_b128 v[164:167], v132 offset:25600
	v_exp_f32_e32 v155, v64
	v_sub_f32_e32 v64, v76, v88
	v_mfma_f32_16x16x32_bf16 v[84:87], v[168:171], v[4:7], v[84:87]
	ds_read_b64_tr_b16 v[168:169], v146 offset:32768
	ds_read_b64_tr_b16 v[170:171], v148 offset:32768
	v_exp_f32_e32 v156, v64
	v_sub_f32_e32 v64, v77, v89
	v_mfma_f32_16x16x32_bf16 v[92:95], v[176:179], v[0:3], v[240:243]
	ds_read_b64_tr_b16 v[178:179], v148 offset:40960
	v_exp_f32_e32 v157, v64
	v_sub_f32_e32 v64, v78, v90
	v_exp_f32_e32 v158, v64
	v_sub_f32_e32 v64, v79, v91
	s_waitcnt lgkmcnt(10)
	v_mfma_f32_16x16x32_bf16 v[88:91], v[184:187], v[4:7], v[92:95]
	ds_read_b64_tr_b16 v[176:177], v146 offset:40960
	ds_read_b64_tr_b16 v[184:185], v139 offset:32768
	ds_read_b64_tr_b16 v[186:187], v142 offset:32768
	v_exp_f32_e32 v159, v64
	v_mfma_f32_16x16x32_bf16 v[80:83], v[172:175], v[8:11], v[84:87]
	ds_read_b64_tr_b16 v[174:175], v142 offset:40960
	ds_read_b64_tr_b16 v[172:173], v139 offset:40960
	v_sub_f32_e32 v64, v72, v66
	v_sub_f32_e32 v70, v73, v67
	v_mfma_f32_16x16x32_bf16 v[76:79], v[188:191], v[8:11], v[88:91]
	v_sub_f32_e32 v68, v74, v68
	s_and_b64 vcc, exec, s[6:7]
	v_mfma_f32_16x16x32_bf16 v[92:95], v[192:195], v[0:3], v[240:243]
	v_mfma_f32_16x16x32_bf16 v[76:79], v[196:199], v[12:15], v[76:79]
	s_waitcnt lgkmcnt(11)
	v_mfma_f32_16x16x32_bf16 v[88:91], v[200:203], v[4:7], v[92:95]
	ds_read_b64_tr_b16 v[188:189], v141 offset:32768
	ds_read_b64_tr_b16 v[190:191], v145 offset:32768
	ds_read_b64_tr_b16 v[194:195], v145 offset:40960
	ds_read_b64_tr_b16 v[192:193], v141 offset:40960
	v_mfma_f32_16x16x32_bf16 v[80:83], v[180:183], v[12:15], v[80:83]
	v_exp_f32_e32 v160, v64
	v_exp_f32_e32 v161, v70
	v_mfma_f32_16x16x32_bf16 v[84:87], v[204:207], v[8:11], v[88:91]
	v_exp_f32_e32 v162, v68
	v_mfma_f32_16x16x32_bf16 v[64:67], v[212:215], v[12:15], v[84:87]
	v_sub_f32_e32 v68, v75, v69
	v_exp_f32_e32 v163, v68
	v_mfma_f32_16x16x32_bf16 v[84:87], v[208:211], v[0:3], v[240:243]
	v_cvt_pk_bf16_f32 v92, v96, v97
	v_cvt_pk_bf16_f32 v93, v98, v99
	s_waitcnt lgkmcnt(11)
	v_mfma_f32_16x16x32_bf16 v[84:87], v[216:219], v[4:7], v[84:87]
	ds_read_b64_tr_b16 v[196:197], v140 offset:32768
	ds_read_b64_tr_b16 v[198:199], v143 offset:32768
	ds_read_b64_tr_b16 v[202:203], v143 offset:40960
	ds_read_b64_tr_b16 v[200:201], v140 offset:40960
	v_cvt_pk_bf16_f32 v94, v152, v153
	v_cvt_pk_bf16_f32 v95, v154, v155
	v_mfma_f32_16x16x32_bf16 v[68:71], v[220:223], v[8:11], v[84:87]
	s_nop 2
	v_cvt_pk_bf16_f32 v84, v156, v157
	v_mfma_f32_16x16x32_bf16 v[68:71], v[164:167], v[12:15], v[68:71]
	v_cvt_pk_bf16_f32 v85, v158, v159
	v_cvt_pk_bf16_f32 v86, v160, v161
	s_waitcnt lgkmcnt(11)
	v_mfma_f32_16x16x32_bf16 v[60:63], v[168:171], v[92:95], v[60:63]
	ds_read_b64_tr_b16 v[180:181], v147 offset:32768
	ds_read_b64_tr_b16 v[182:183], v149 offset:32768
	ds_read_b64_tr_b16 v[206:207], v149 offset:40960
	ds_read_b64_tr_b16 v[204:205], v147 offset:40960
	v_cvt_pk_bf16_f32 v87, v162, v163
	s_nop 1
	v_mfma_f32_16x16x32_bf16 v[60:63], v[176:179], v[84:87], v[60:63]
	s_waitcnt lgkmcnt(11)
	v_mfma_f32_16x16x32_bf16 v[56:59], v[184:187], v[92:95], v[56:59]
	ds_read_b64_tr_b16 v[212:213], v133 offset:32768
	ds_read_b64_tr_b16 v[214:215], v134 offset:32768
	ds_read_b64_tr_b16 v[210:211], v134 offset:40960
	ds_read_b64_tr_b16 v[208:209], v133 offset:40960
	v_mfma_f32_16x16x32_bf16 v[56:59], v[172:175], v[84:87], v[56:59]
	s_waitcnt lgkmcnt(11)
	v_mfma_f32_16x16x32_bf16 v[52:55], v[188:191], v[92:95], v[52:55]
	ds_read_b64_tr_b16 v[216:217], v135 offset:32768
	ds_read_b64_tr_b16 v[218:219], v136 offset:32768
	ds_read_b64_tr_b16 v[222:223], v136 offset:40960
	ds_read_b64_tr_b16 v[220:221], v135 offset:40960
	v_mfma_f32_16x16x32_bf16 v[52:55], v[192:195], v[84:87], v[52:55]
	s_waitcnt lgkmcnt(11)
	v_mfma_f32_16x16x32_bf16 v[48:51], v[196:199], v[92:95], v[48:51]
	ds_read_b64_tr_b16 v[164:165], v137 offset:32768
	ds_read_b64_tr_b16 v[166:167], v138 offset:32768
	ds_read_b64_tr_b16 v[170:171], v138 offset:40960
	ds_read_b64_tr_b16 v[168:169], v137 offset:40960
	v_mfma_f32_16x16x32_bf16 v[48:51], v[200:203], v[84:87], v[48:51]
	s_waitcnt lgkmcnt(11)
	v_mfma_f32_16x16x32_bf16 v[32:35], v[180:183], v[92:95], v[32:35]
	v_mfma_f32_16x16x32_bf16 v[32:35], v[204:207], v[84:87], v[32:35]
	s_waitcnt lgkmcnt(7)
	v_mfma_f32_16x16x32_bf16 v[36:39], v[212:215], v[92:95], v[36:39]
	v_mfma_f32_16x16x32_bf16 v[36:39], v[208:211], v[84:87], v[36:39]
	s_waitcnt lgkmcnt(3)
	v_mfma_f32_16x16x32_bf16 v[40:43], v[216:219], v[92:95], v[40:43]
	v_mfma_f32_16x16x32_bf16 v[40:43], v[220:223], v[84:87], v[40:43]
	s_waitcnt lgkmcnt(0)
	v_mfma_f32_16x16x32_bf16 v[44:47], v[164:167], v[92:95], v[44:47]
	v_mfma_f32_16x16x32_bf16 v[44:47], v[168:171], v[84:87], v[44:47]
	s_cbranch_vccnz .LBB0_1968
	v_add_u32_e32 v72, 0, v109
	s_waitcnt vmcnt(3)
	ds_write_b128 v100, v[16:19]
	s_waitcnt vmcnt(2)
	ds_write_b128 v124, v[20:23]
	s_waitcnt vmcnt(1)
	ds_write_b128 v72, v[24:27] offset:49152
	v_add_u32_e32 v72, 0, v112
	s_waitcnt vmcnt(0)
	ds_write_b128 v72, v[28:31] offset:49152

.LBB0_2030:
	ds_read_b128 v[88:91], v128
	ds_read_b128 v[92:95], v128 offset:1024
	ds_read_b128 v[156:159], v129
	ds_read_b128 v[188:191], v129 offset:1024
	ds_read_b128 v[192:195], v130
	ds_read_b128 v[196:199], v130 offset:1024
	ds_read_b128 v[200:203], v131
	ds_read_b128 v[204:207], v131 offset:1024
	ds_read_b128 v[208:211], v128 offset:8192
	ds_read_b128 v[212:215], v128 offset:9216
	ds_read_b128 v[216:219], v129 offset:8192
	ds_read_b128 v[220:223], v129 offset:9216
	s_and_b64 vcc, exec, s[6:7]
	s_waitcnt lgkmcnt(8)
	v_mfma_f32_16x16x32_bf16 v[72:75], v[88:91], v[0:3], 0
	ds_read_b128 v[88:91], v130 offset:8192
	v_mfma_f32_16x16x32_bf16 v[80:83], v[92:95], v[0:3], 0
	ds_read_b128 v[92:95], v130 offset:9216
	v_mfma_f32_16x16x32_bf16 v[72:75], v[156:159], v[4:7], v[72:75]
	ds_read_b128 v[156:159], v131 offset:8192
	s_waitcnt lgkmcnt(7)
	v_mfma_f32_16x16x32_bf16 v[72:75], v[192:195], v[8:11], v[72:75]
	ds_read_b128 v[192:195], v131 offset:9216
	v_mfma_f32_16x16x32_bf16 v[76:79], v[200:203], v[12:15], v[72:75]
	ds_read_b64_tr_b16 v[200:201], v140 offset:49152
	ds_read_b64_tr_b16 v[202:203], v141 offset:49152
	v_mfma_f32_16x16x32_bf16 v[72:75], v[188:191], v[4:7], v[80:83]
	ds_read_b64_tr_b16 v[190:191], v141 offset:57344
	ds_read_b64_tr_b16 v[188:189], v140 offset:57344
	v_mfma_f32_16x16x32_bf16 v[72:75], v[196:199], v[8:11], v[72:75]
	ds_read_b64_tr_b16 v[196:197], v136 offset:49152
	ds_read_b64_tr_b16 v[198:199], v137 offset:49152
	v_mfma_f32_16x16x32_bf16 v[72:75], v[204:207], v[12:15], v[72:75]
	ds_read_b64_tr_b16 v[206:207], v137 offset:57344
	s_waitcnt lgkmcnt(11)
	v_mfma_f32_16x16x32_bf16 v[80:83], v[208:211], v[0:3], 0
	ds_read_b64_tr_b16 v[204:205], v136 offset:57344
	ds_read_b64_tr_b16 v[208:209], v138 offset:49152
	ds_read_b64_tr_b16 v[210:211], v142 offset:49152
	v_mfma_f32_16x16x32_bf16 v[80:83], v[216:219], v[4:7], v[80:83]
	ds_read_b64_tr_b16 v[218:219], v142 offset:57344
	s_waitcnt lgkmcnt(11)
	v_mfma_f32_16x16x32_bf16 v[80:83], v[88:91], v[8:11], v[80:83]
	ds_read_b64_tr_b16 v[216:217], v138 offset:57344
	ds_read_b64_tr_b16 v[88:89], v139 offset:49152
	ds_read_b64_tr_b16 v[90:91], v143 offset:49152
	v_mfma_f32_16x16x32_bf16 v[84:87], v[156:159], v[12:15], v[80:83]
	ds_read_b64_tr_b16 v[158:159], v143 offset:57344
	v_mfma_f32_16x16x32_bf16 v[80:83], v[212:215], v[0:3], 0
	v_mfma_f32_16x16x32_bf16 v[80:83], v[220:223], v[4:7], v[80:83]
	s_waitcnt lgkmcnt(10)
	v_mfma_f32_16x16x32_bf16 v[48:51], v[200:203], v[68:71], v[48:51]
	ds_read_b64_tr_b16 v[156:157], v139 offset:57344
	ds_read_b64_tr_b16 v[212:213], v145 offset:49152
	ds_read_b64_tr_b16 v[214:215], v146 offset:49152
	ds_read_b64_tr_b16 v[222:223], v146 offset:57344
	ds_read_b64_tr_b16 v[220:221], v145 offset:57344
	v_mfma_f32_16x16x32_bf16 v[48:51], v[188:191], v[64:67], v[48:51]
	s_waitcnt lgkmcnt(11)
	v_mfma_f32_16x16x32_bf16 v[40:43], v[196:199], v[68:71], v[40:43]
	ds_read_b64_tr_b16 v[200:201], v147 offset:49152
	ds_read_b64_tr_b16 v[202:203], v148 offset:49152
	ds_read_b64_tr_b16 v[190:191], v148 offset:57344
	ds_read_b64_tr_b16 v[188:189], v147 offset:57344
	v_mfma_f32_16x16x32_bf16 v[40:43], v[204:207], v[64:67], v[40:43]
	s_waitcnt lgkmcnt(11)
	v_mfma_f32_16x16x32_bf16 v[44:47], v[208:211], v[68:71], v[44:47]
	ds_read_b64_tr_b16 v[196:197], v149 offset:49152
	ds_read_b64_tr_b16 v[198:199], v150 offset:49152
	ds_read_b64_tr_b16 v[206:207], v150 offset:57344
	ds_read_b64_tr_b16 v[204:205], v149 offset:57344
	v_mfma_f32_16x16x32_bf16 v[44:47], v[216:219], v[64:67], v[44:47]
	s_waitcnt lgkmcnt(11)
	v_mfma_f32_16x16x32_bf16 v[56:59], v[88:91], v[68:71], v[56:59]
	ds_read_b64_tr_b16 v[208:209], v151 offset:49152
	ds_read_b64_tr_b16 v[210:211], v152 offset:49152
	ds_read_b64_tr_b16 v[218:219], v152 offset:57344
	ds_read_b64_tr_b16 v[216:217], v151 offset:57344
	v_mfma_f32_16x16x32_bf16 v[56:59], v[156:159], v[64:67], v[56:59]
	s_waitcnt lgkmcnt(11)
	v_mfma_f32_16x16x32_bf16 v[60:63], v[212:215], v[68:71], v[60:63]
	v_mfma_f32_16x16x32_bf16 v[60:63], v[220:223], v[64:67], v[60:63]
	s_waitcnt lgkmcnt(7)
	v_mfma_f32_16x16x32_bf16 v[52:55], v[200:203], v[68:71], v[52:55]
	v_mfma_f32_16x16x32_bf16 v[52:55], v[188:191], v[64:67], v[52:55]
	s_waitcnt lgkmcnt(3)
	v_mfma_f32_16x16x32_bf16 v[32:35], v[196:199], v[68:71], v[32:35]
	v_mfma_f32_16x16x32_bf16 v[32:35], v[204:207], v[64:67], v[32:35]
	v_mfma_f32_16x16x32_bf16 v[80:83], v[92:95], v[8:11], v[80:83]
	s_waitcnt lgkmcnt(0)
	v_mfma_f32_16x16x32_bf16 v[36:39], v[208:211], v[68:71], v[36:39]
	v_mfma_f32_16x16x32_bf16 v[80:83], v[192:195], v[12:15], v[80:83]
	v_mfma_f32_16x16x32_bf16 v[36:39], v[216:219], v[64:67], v[36:39]
	s_cbranch_vccnz .LBB0_2032
	s_waitcnt vmcnt(3)
	ds_write_b128 v98, v[16:19] offset:16384
	s_waitcnt vmcnt(2)
	ds_write_b128 v99, v[20:23] offset:16384
	s_waitcnt vmcnt(1)
	ds_write_b128 v100, v[24:27] offset:32768
	s_waitcnt vmcnt(0)
	ds_write_b128 v124, v[28:31] offset:32768

.LBB0_2054:
	ds_read_b128 v[176:179], v128 offset:16384
	ds_read_b128 v[180:183], v128 offset:17408
	ds_read_b128 v[188:191], v129 offset:16384
	ds_read_b128 v[192:195], v130 offset:16384
	ds_read_b128 v[196:199], v131 offset:16384
	ds_read_b128 v[200:203], v129 offset:17408
	ds_read_b128 v[204:207], v130 offset:17408
	ds_read_b128 v[208:211], v129 offset:24576
	ds_read_b128 v[212:215], v131 offset:17408
	ds_read_b128 v[216:219], v128 offset:24576
	ds_read_b128 v[220:223], v130 offset:24576
	v_pk_mul_f32 v[184:185], v[66:67], v[68:69]
	s_waitcnt lgkmcnt(7)
	v_mfma_f32_16x16x32_bf16 v[160:163], v[176:179], v[0:3], 0
	ds_read_b128 v[176:179], v128 offset:25600
	v_mul_f32_e32 v70, v70, v71
	v_mul_f32_e32 v157, v70, v157
	v_mul_f32_e32 v159, v157, v159
	v_mfma_f32_16x16x32_bf16 v[164:167], v[180:183], v[0:3], 0
	ds_read_b128 v[180:183], v131 offset:24576
	v_mul_f32_e32 v186, v153, v159
	v_pk_mul_f32 v[64:65], v[64:65], v[96:97]
	v_pk_mul_f32 v[72:73], v[72:73], v[74:75]
	v_mfma_f32_16x16x32_bf16 v[160:163], v[188:191], v[4:7], v[160:163]
	ds_read_b128 v[188:191], v129 offset:25600
	v_pk_mul_f32 v[96:97], v[64:65], v[186:187] op_sel_hi:[1,0]
	v_pk_mul_f32 v[84:85], v[84:85], v[94:95]
	v_mfma_f32_16x16x32_bf16 v[66:69], v[192:195], v[8:11], v[160:163]
	ds_read_b128 v[192:195], v130 offset:25600
	v_cvt_pk_bf16_f32 v173, v96, v97
	v_pk_mul_f32 v[96:97], v[76:77], v[78:79]
	s_waitcnt lgkmcnt(7)
	v_mfma_f32_16x16x32_bf16 v[68:71], v[196:199], v[12:15], v[66:69]
	ds_read_b128 v[196:199], v131 offset:25600
	v_pk_mul_f32 v[96:97], v[96:97], v[186:187] op_sel_hi:[1,0]
	v_pk_mul_f32 v[86:87], v[86:87], v[92:93]
	v_mfma_f32_16x16x32_bf16 v[164:167], v[200:203], v[4:7], v[164:167]
	ds_read_b64_tr_b16 v[200:201], v140 offset:32768
	ds_read_b64_tr_b16 v[202:203], v141 offset:32768
	v_mul_f32_e64 v66, v184, v186
	v_mul_f32_e64 v67, v185, v186
	v_pk_mul_f32 v[80:81], v[80:81], v[82:83]
	v_cvt_pk_bf16_f32 v172, v66, v67
	v_mfma_f32_16x16x32_bf16 v[64:67], v[204:207], v[8:11], v[164:167]
	ds_read_b64_tr_b16 v[206:207], v141 offset:40960
	ds_read_b64_tr_b16 v[204:205], v140 offset:40960
	s_and_b64 vcc, exec, s[6:7]
	s_waitcnt lgkmcnt(8)
	v_mfma_f32_16x16x32_bf16 v[64:67], v[212:215], v[12:15], v[64:67]
	ds_read_b64_tr_b16 v[212:213], v136 offset:32768
	ds_read_b64_tr_b16 v[214:215], v137 offset:32768
	v_mfma_f32_16x16x32_bf16 v[168:171], v[216:219], v[0:3], 0
	ds_read_b64_tr_b16 v[218:219], v137 offset:40960
	ds_read_b64_tr_b16 v[216:217], v136 offset:40960
	v_cvt_pk_bf16_f32 v174, v96, v97
	v_pk_mul_f32 v[96:97], v[72:73], v[186:187] op_sel_hi:[1,0]
	v_mfma_f32_16x16x32_bf16 v[76:79], v[208:211], v[4:7], v[168:171]
	ds_read_b64_tr_b16 v[208:209], v138 offset:32768
	ds_read_b64_tr_b16 v[210:211], v142 offset:32768
	v_cvt_pk_bf16_f32 v175, v96, v97
	v_mfma_f32_16x16x32_bf16 v[94:97], v[176:179], v[0:3], 0
	ds_read_b64_tr_b16 v[178:179], v142 offset:40960
	v_mfma_f32_16x16x32_bf16 v[72:75], v[220:223], v[8:11], v[76:79]
	v_mul_f32_e32 v162, v153, v158
	v_pk_mul_f32 v[84:85], v[84:85], v[162:163] op_sel_hi:[1,0]
	v_pk_mul_f32 v[86:87], v[86:87], v[162:163] op_sel_hi:[1,0]
	s_waitcnt lgkmcnt(10)
	v_mfma_f32_16x16x32_bf16 v[92:95], v[188:191], v[4:7], v[94:97]
	ds_read_b64_tr_b16 v[176:177], v138 offset:40960
	ds_read_b64_tr_b16 v[220:221], v139 offset:32768
	ds_read_b64_tr_b16 v[222:223], v143 offset:32768
	ds_read_b64_tr_b16 v[190:191], v143 offset:40960
	ds_read_b64_tr_b16 v[188:189], v139 offset:40960
	v_cvt_pk_bf16_f32 v84, v84, v85
	v_cvt_pk_bf16_f32 v85, v86, v87
	v_pk_mul_f32 v[86:87], v[88:89], v[90:91]
	v_mfma_f32_16x16x32_bf16 v[92:95], v[192:195], v[8:11], v[92:95]
	v_pk_mul_f32 v[86:87], v[86:87], v[162:163] op_sel_hi:[1,0]
	v_mfma_f32_16x16x32_bf16 v[76:79], v[196:199], v[12:15], v[92:95]
	v_cvt_pk_bf16_f32 v86, v86, v87
	s_nop 4
	v_pk_mul_f32 v[92:93], v[80:81], v[162:163] op_sel_hi:[1,0]
	s_waitcnt lgkmcnt(11)
	v_mfma_f32_16x16x32_bf16 v[48:51], v[200:203], v[172:175], v[48:51]
	ds_read_b64_tr_b16 v[192:193], v145 offset:32768
	ds_read_b64_tr_b16 v[194:195], v146 offset:32768
	ds_read_b64_tr_b16 v[198:199], v146 offset:40960
	ds_read_b64_tr_b16 v[196:197], v145 offset:40960
	v_cvt_pk_bf16_f32 v87, v92, v93
	s_waitcnt lgkmcnt(11)
	v_mfma_f32_16x16x32_bf16 v[40:43], v[212:215], v[172:175], v[40:43]
	ds_read_b64_tr_b16 v[200:201], v147 offset:32768
	ds_read_b64_tr_b16 v[202:203], v148 offset:32768
	ds_read_b64_tr_b16 v[214:215], v148 offset:40960
	ds_read_b64_tr_b16 v[212:213], v147 offset:40960
	v_mfma_f32_16x16x32_bf16 v[40:43], v[216:219], v[84:87], v[40:43]
	s_waitcnt lgkmcnt(11)
	v_mfma_f32_16x16x32_bf16 v[44:47], v[208:211], v[172:175], v[44:47]
	ds_read_b64_tr_b16 v[216:217], v149 offset:32768
	ds_read_b64_tr_b16 v[218:219], v150 offset:32768
	ds_read_b64_tr_b16 v[210:211], v150 offset:40960
	ds_read_b64_tr_b16 v[208:209], v149 offset:40960
	v_mfma_f32_16x16x32_bf16 v[44:47], v[176:179], v[84:87], v[44:47]
	s_waitcnt lgkmcnt(11)
	v_mfma_f32_16x16x32_bf16 v[56:59], v[220:223], v[172:175], v[56:59]
	ds_read_b64_tr_b16 v[176:177], v151 offset:32768
	ds_read_b64_tr_b16 v[178:179], v152 offset:32768
	ds_read_b64_tr_b16 v[222:223], v152 offset:40960
	ds_read_b64_tr_b16 v[220:221], v151 offset:40960
	v_mfma_f32_16x16x32_bf16 v[56:59], v[188:191], v[84:87], v[56:59]
	s_waitcnt lgkmcnt(11)
	v_mfma_f32_16x16x32_bf16 v[60:63], v[192:195], v[172:175], v[60:63]
	v_mfma_f32_16x16x32_bf16 v[60:63], v[196:199], v[84:87], v[60:63]
	s_waitcnt lgkmcnt(7)
	v_mfma_f32_16x16x32_bf16 v[52:55], v[200:203], v[172:175], v[52:55]
	v_mfma_f32_16x16x32_bf16 v[52:55], v[212:215], v[84:87], v[52:55]
	s_waitcnt lgkmcnt(3)
	v_mfma_f32_16x16x32_bf16 v[32:35], v[216:219], v[172:175], v[32:35]
	v_mfma_f32_16x16x32_bf16 v[32:35], v[208:211], v[84:87], v[32:35]
	s_waitcnt lgkmcnt(0)
	v_mfma_f32_16x16x32_bf16 v[36:39], v[176:179], v[172:175], v[36:39]
	v_mfma_f32_16x16x32_bf16 v[72:75], v[180:183], v[12:15], v[72:75]
	v_mfma_f32_16x16x32_bf16 v[48:51], v[204:207], v[84:87], v[48:51]
	v_mfma_f32_16x16x32_bf16 v[36:39], v[220:223], v[84:87], v[36:39]
	s_cbranch_vccnz .LBB0_2056
	s_waitcnt vmcnt(3)
	ds_write_b128 v98, v[16:19]
	s_waitcnt vmcnt(2)
	ds_write_b128 v99, v[20:23]
	s_waitcnt vmcnt(1)
	ds_write_b128 v100, v[24:27] offset:49152
	s_waitcnt vmcnt(0)
	ds_write_b128 v124, v[28:31] offset:49152

.LBB0_2133:
	ds_read_b128 v[88:91], v128
	ds_read_b128 v[92:95], v128 offset:1024
	ds_read_b128 v[156:159], v129
	ds_read_b128 v[188:191], v129 offset:1024
	ds_read_b128 v[192:195], v130
	ds_read_b128 v[196:199], v130 offset:1024
	ds_read_b128 v[200:203], v131
	ds_read_b128 v[204:207], v131 offset:1024
	ds_read_b128 v[208:211], v128 offset:8192
	ds_read_b128 v[212:215], v128 offset:9216
	ds_read_b128 v[216:219], v129 offset:8192
	ds_read_b128 v[220:223], v129 offset:9216
	s_and_b64 vcc, exec, s[6:7]
	s_waitcnt lgkmcnt(8)
	v_mfma_f32_16x16x32_bf16 v[72:75], v[88:91], v[0:3], 0
	ds_read_b128 v[88:91], v130 offset:8192
	v_mfma_f32_16x16x32_bf16 v[80:83], v[92:95], v[0:3], 0
	ds_read_b128 v[92:95], v130 offset:9216
	v_mfma_f32_16x16x32_bf16 v[72:75], v[156:159], v[4:7], v[72:75]
	ds_read_b128 v[156:159], v131 offset:8192
	s_waitcnt lgkmcnt(7)
	v_mfma_f32_16x16x32_bf16 v[72:75], v[192:195], v[8:11], v[72:75]
	ds_read_b128 v[192:195], v131 offset:9216
	v_mfma_f32_16x16x32_bf16 v[76:79], v[200:203], v[12:15], v[72:75]
	ds_read_b64_tr_b16 v[200:201], v142 offset:49152
	ds_read_b64_tr_b16 v[202:203], v143 offset:49152
	v_mfma_f32_16x16x32_bf16 v[72:75], v[188:191], v[4:7], v[80:83]
	ds_read_b64_tr_b16 v[190:191], v143 offset:57344
	ds_read_b64_tr_b16 v[188:189], v142 offset:57344
	v_mfma_f32_16x16x32_bf16 v[72:75], v[196:199], v[8:11], v[72:75]
	ds_read_b64_tr_b16 v[196:197], v136 offset:49152
	ds_read_b64_tr_b16 v[198:199], v139 offset:49152
	v_mfma_f32_16x16x32_bf16 v[72:75], v[204:207], v[12:15], v[72:75]
	ds_read_b64_tr_b16 v[206:207], v139 offset:57344
	s_waitcnt lgkmcnt(11)
	v_mfma_f32_16x16x32_bf16 v[80:83], v[208:211], v[0:3], 0
	ds_read_b64_tr_b16 v[204:205], v136 offset:57344
	ds_read_b64_tr_b16 v[208:209], v138 offset:49152
	ds_read_b64_tr_b16 v[210:211], v141 offset:49152
	v_mfma_f32_16x16x32_bf16 v[80:83], v[216:219], v[4:7], v[80:83]
	ds_read_b64_tr_b16 v[218:219], v141 offset:57344
	s_waitcnt lgkmcnt(11)
	v_mfma_f32_16x16x32_bf16 v[80:83], v[88:91], v[8:11], v[80:83]
	ds_read_b64_tr_b16 v[216:217], v138 offset:57344
	ds_read_b64_tr_b16 v[88:89], v137 offset:49152
	ds_read_b64_tr_b16 v[90:91], v140 offset:49152
	v_mfma_f32_16x16x32_bf16 v[84:87], v[156:159], v[12:15], v[80:83]
	ds_read_b64_tr_b16 v[158:159], v140 offset:57344
	v_mfma_f32_16x16x32_bf16 v[80:83], v[212:215], v[0:3], 0
	v_mfma_f32_16x16x32_bf16 v[80:83], v[220:223], v[4:7], v[80:83]
	s_waitcnt lgkmcnt(10)
	v_mfma_f32_16x16x32_bf16 v[60:63], v[200:203], v[64:67], v[60:63]
	ds_read_b64_tr_b16 v[156:157], v137 offset:57344
	ds_read_b64_tr_b16 v[212:213], v145 offset:49152
	ds_read_b64_tr_b16 v[214:215], v146 offset:49152
	ds_read_b64_tr_b16 v[222:223], v146 offset:57344
	ds_read_b64_tr_b16 v[220:221], v145 offset:57344
	v_mfma_f32_16x16x32_bf16 v[60:63], v[188:191], v[68:71], v[60:63]
	s_waitcnt lgkmcnt(11)
	v_mfma_f32_16x16x32_bf16 v[52:55], v[196:199], v[64:67], v[52:55]
	ds_read_b64_tr_b16 v[200:201], v147 offset:49152
	ds_read_b64_tr_b16 v[202:203], v148 offset:49152
	ds_read_b64_tr_b16 v[190:191], v148 offset:57344
	ds_read_b64_tr_b16 v[188:189], v147 offset:57344
	v_mfma_f32_16x16x32_bf16 v[52:55], v[204:207], v[68:71], v[52:55]
	s_waitcnt lgkmcnt(11)
	v_mfma_f32_16x16x32_bf16 v[44:47], v[208:211], v[64:67], v[44:47]
	ds_read_b64_tr_b16 v[196:197], v149 offset:49152
	ds_read_b64_tr_b16 v[198:199], v150 offset:49152
	ds_read_b64_tr_b16 v[206:207], v150 offset:57344
	ds_read_b64_tr_b16 v[204:205], v149 offset:57344
	v_mfma_f32_16x16x32_bf16 v[44:47], v[216:219], v[68:71], v[44:47]
	s_waitcnt lgkmcnt(11)
	v_mfma_f32_16x16x32_bf16 v[56:59], v[88:91], v[64:67], v[56:59]
	ds_read_b64_tr_b16 v[208:209], v151 offset:49152
	ds_read_b64_tr_b16 v[210:211], v152 offset:49152
	ds_read_b64_tr_b16 v[218:219], v152 offset:57344
	ds_read_b64_tr_b16 v[216:217], v151 offset:57344
	v_mfma_f32_16x16x32_bf16 v[56:59], v[156:159], v[68:71], v[56:59]
	s_waitcnt lgkmcnt(11)
	v_mfma_f32_16x16x32_bf16 v[48:51], v[212:215], v[64:67], v[48:51]
	v_mfma_f32_16x16x32_bf16 v[48:51], v[220:223], v[68:71], v[48:51]
	s_waitcnt lgkmcnt(7)
	v_mfma_f32_16x16x32_bf16 v[40:43], v[200:203], v[64:67], v[40:43]
	v_mfma_f32_16x16x32_bf16 v[40:43], v[188:191], v[68:71], v[40:43]
	s_waitcnt lgkmcnt(3)
	v_mfma_f32_16x16x32_bf16 v[32:35], v[196:199], v[64:67], v[32:35]
	v_mfma_f32_16x16x32_bf16 v[32:35], v[204:207], v[68:71], v[32:35]
	v_mfma_f32_16x16x32_bf16 v[80:83], v[92:95], v[8:11], v[80:83]
	s_waitcnt lgkmcnt(0)
	v_mfma_f32_16x16x32_bf16 v[36:39], v[208:211], v[64:67], v[36:39]
	v_mfma_f32_16x16x32_bf16 v[80:83], v[192:195], v[12:15], v[80:83]
	v_mfma_f32_16x16x32_bf16 v[36:39], v[216:219], v[68:71], v[36:39]
	s_cbranch_vccnz .LBB0_2135
	s_waitcnt vmcnt(3)
	ds_write_b128 v98, v[16:19] offset:16384
	s_waitcnt vmcnt(2)
	ds_write_b128 v99, v[20:23] offset:16384
	s_waitcnt vmcnt(1)
	ds_write_b128 v100, v[24:27] offset:32768
	s_waitcnt vmcnt(0)
	ds_write_b128 v124, v[28:31] offset:32768

.LBB0_2157:
	ds_read_b128 v[176:179], v128 offset:16384
	ds_read_b128 v[180:183], v128 offset:17408
	ds_read_b128 v[188:191], v129 offset:16384
	ds_read_b128 v[192:195], v130 offset:16384
	ds_read_b128 v[196:199], v131 offset:16384
	ds_read_b128 v[200:203], v129 offset:17408
	ds_read_b128 v[204:207], v130 offset:17408
	ds_read_b128 v[208:211], v129 offset:24576
	ds_read_b128 v[212:215], v131 offset:17408
	ds_read_b128 v[216:219], v128 offset:24576
	ds_read_b128 v[220:223], v130 offset:24576
	v_pk_mul_f32 v[184:185], v[66:67], v[68:69]
	s_waitcnt lgkmcnt(7)
	v_mfma_f32_16x16x32_bf16 v[160:163], v[176:179], v[0:3], 0
	ds_read_b128 v[176:179], v128 offset:25600
	v_mul_f32_e32 v70, v70, v71
	v_mul_f32_e32 v157, v70, v157
	v_mul_f32_e32 v159, v157, v159
	v_mfma_f32_16x16x32_bf16 v[164:167], v[180:183], v[0:3], 0
	ds_read_b128 v[180:183], v131 offset:24576
	v_mul_f32_e32 v186, v153, v159
	v_pk_mul_f32 v[64:65], v[64:65], v[96:97]
	v_pk_mul_f32 v[72:73], v[72:73], v[74:75]
	v_mfma_f32_16x16x32_bf16 v[160:163], v[188:191], v[4:7], v[160:163]
	ds_read_b128 v[188:191], v129 offset:25600
	v_pk_mul_f32 v[96:97], v[64:65], v[186:187] op_sel_hi:[1,0]
	v_pk_mul_f32 v[84:85], v[84:85], v[94:95]
	v_mfma_f32_16x16x32_bf16 v[66:69], v[192:195], v[8:11], v[160:163]
	ds_read_b128 v[192:195], v130 offset:25600
	v_cvt_pk_bf16_f32 v173, v96, v97
	v_pk_mul_f32 v[96:97], v[76:77], v[78:79]
	s_waitcnt lgkmcnt(7)
	v_mfma_f32_16x16x32_bf16 v[68:71], v[196:199], v[12:15], v[66:69]
	ds_read_b128 v[196:199], v131 offset:25600
	v_pk_mul_f32 v[96:97], v[96:97], v[186:187] op_sel_hi:[1,0]
	v_pk_mul_f32 v[86:87], v[86:87], v[92:93]
	v_mfma_f32_16x16x32_bf16 v[164:167], v[200:203], v[4:7], v[164:167]
	ds_read_b64_tr_b16 v[200:201], v142 offset:32768
	ds_read_b64_tr_b16 v[202:203], v143 offset:32768
	v_mul_f32_e64 v66, v184, v186
	v_mul_f32_e64 v67, v185, v186
	v_pk_mul_f32 v[80:81], v[80:81], v[82:83]
	v_cvt_pk_bf16_f32 v172, v66, v67
	v_mfma_f32_16x16x32_bf16 v[64:67], v[204:207], v[8:11], v[164:167]
	ds_read_b64_tr_b16 v[206:207], v143 offset:40960
	ds_read_b64_tr_b16 v[204:205], v142 offset:40960
	s_and_b64 vcc, exec, s[6:7]
	s_waitcnt lgkmcnt(8)
	v_mfma_f32_16x16x32_bf16 v[64:67], v[212:215], v[12:15], v[64:67]
	ds_read_b64_tr_b16 v[212:213], v136 offset:32768
	ds_read_b64_tr_b16 v[214:215], v139 offset:32768
	v_mfma_f32_16x16x32_bf16 v[168:171], v[216:219], v[0:3], 0
	ds_read_b64_tr_b16 v[218:219], v139 offset:40960
	ds_read_b64_tr_b16 v[216:217], v136 offset:40960
	v_cvt_pk_bf16_f32 v174, v96, v97
	v_pk_mul_f32 v[96:97], v[72:73], v[186:187] op_sel_hi:[1,0]
	v_mfma_f32_16x16x32_bf16 v[76:79], v[208:211], v[4:7], v[168:171]
	ds_read_b64_tr_b16 v[208:209], v138 offset:32768
	ds_read_b64_tr_b16 v[210:211], v141 offset:32768
	v_cvt_pk_bf16_f32 v175, v96, v97
	v_mfma_f32_16x16x32_bf16 v[94:97], v[176:179], v[0:3], 0
	ds_read_b64_tr_b16 v[178:179], v141 offset:40960
	v_mfma_f32_16x16x32_bf16 v[72:75], v[220:223], v[8:11], v[76:79]
	v_mul_f32_e32 v162, v153, v158
	v_pk_mul_f32 v[84:85], v[84:85], v[162:163] op_sel_hi:[1,0]
	v_pk_mul_f32 v[86:87], v[86:87], v[162:163] op_sel_hi:[1,0]
	s_waitcnt lgkmcnt(10)
	v_mfma_f32_16x16x32_bf16 v[92:95], v[188:191], v[4:7], v[94:97]
	ds_read_b64_tr_b16 v[176:177], v138 offset:40960
	ds_read_b64_tr_b16 v[220:221], v137 offset:32768
	ds_read_b64_tr_b16 v[222:223], v140 offset:32768
	ds_read_b64_tr_b16 v[190:191], v140 offset:40960
	ds_read_b64_tr_b16 v[188:189], v137 offset:40960
	v_cvt_pk_bf16_f32 v84, v84, v85
	v_cvt_pk_bf16_f32 v85, v86, v87
	v_pk_mul_f32 v[86:87], v[88:89], v[90:91]
	v_mfma_f32_16x16x32_bf16 v[92:95], v[192:195], v[8:11], v[92:95]
	v_pk_mul_f32 v[86:87], v[86:87], v[162:163] op_sel_hi:[1,0]
	v_mfma_f32_16x16x32_bf16 v[76:79], v[196:199], v[12:15], v[92:95]
	v_cvt_pk_bf16_f32 v86, v86, v87
	s_nop 4
	v_pk_mul_f32 v[92:93], v[80:81], v[162:163] op_sel_hi:[1,0]
	s_waitcnt lgkmcnt(11)
	v_mfma_f32_16x16x32_bf16 v[60:63], v[200:203], v[172:175], v[60:63]
	ds_read_b64_tr_b16 v[192:193], v145 offset:32768
	ds_read_b64_tr_b16 v[194:195], v146 offset:32768
	ds_read_b64_tr_b16 v[198:199], v146 offset:40960
	ds_read_b64_tr_b16 v[196:197], v145 offset:40960
	v_cvt_pk_bf16_f32 v87, v92, v93
	s_waitcnt lgkmcnt(11)
	v_mfma_f32_16x16x32_bf16 v[52:55], v[212:215], v[172:175], v[52:55]
	ds_read_b64_tr_b16 v[200:201], v147 offset:32768
	ds_read_b64_tr_b16 v[202:203], v148 offset:32768
	ds_read_b64_tr_b16 v[214:215], v148 offset:40960
	ds_read_b64_tr_b16 v[212:213], v147 offset:40960
	v_mfma_f32_16x16x32_bf16 v[52:55], v[216:219], v[84:87], v[52:55]
	s_waitcnt lgkmcnt(11)
	v_mfma_f32_16x16x32_bf16 v[44:47], v[208:211], v[172:175], v[44:47]
	ds_read_b64_tr_b16 v[216:217], v149 offset:32768
	ds_read_b64_tr_b16 v[218:219], v150 offset:32768
	ds_read_b64_tr_b16 v[210:211], v150 offset:40960
	ds_read_b64_tr_b16 v[208:209], v149 offset:40960
	v_mfma_f32_16x16x32_bf16 v[44:47], v[176:179], v[84:87], v[44:47]
	s_waitcnt lgkmcnt(11)
	v_mfma_f32_16x16x32_bf16 v[56:59], v[220:223], v[172:175], v[56:59]
	ds_read_b64_tr_b16 v[176:177], v151 offset:32768
	ds_read_b64_tr_b16 v[178:179], v152 offset:32768
	ds_read_b64_tr_b16 v[222:223], v152 offset:40960
	ds_read_b64_tr_b16 v[220:221], v151 offset:40960
	v_mfma_f32_16x16x32_bf16 v[56:59], v[188:191], v[84:87], v[56:59]
	s_waitcnt lgkmcnt(11)
	v_mfma_f32_16x16x32_bf16 v[48:51], v[192:195], v[172:175], v[48:51]
	v_mfma_f32_16x16x32_bf16 v[48:51], v[196:199], v[84:87], v[48:51]
	s_waitcnt lgkmcnt(7)
	v_mfma_f32_16x16x32_bf16 v[40:43], v[200:203], v[172:175], v[40:43]
	v_mfma_f32_16x16x32_bf16 v[40:43], v[212:215], v[84:87], v[40:43]
	s_waitcnt lgkmcnt(3)
	v_mfma_f32_16x16x32_bf16 v[32:35], v[216:219], v[172:175], v[32:35]
	v_mfma_f32_16x16x32_bf16 v[32:35], v[208:211], v[84:87], v[32:35]
	s_waitcnt lgkmcnt(0)
	v_mfma_f32_16x16x32_bf16 v[36:39], v[176:179], v[172:175], v[36:39]
	v_mfma_f32_16x16x32_bf16 v[72:75], v[180:183], v[12:15], v[72:75]
	v_mfma_f32_16x16x32_bf16 v[60:63], v[204:207], v[84:87], v[60:63]
	v_mfma_f32_16x16x32_bf16 v[36:39], v[220:223], v[84:87], v[36:39]
	s_cbranch_vccnz .LBB0_2159
	s_waitcnt vmcnt(3)
	ds_write_b128 v98, v[16:19]
	s_waitcnt vmcnt(2)
	ds_write_b128 v99, v[20:23]
	s_waitcnt vmcnt(1)
	ds_write_b128 v100, v[24:27] offset:49152
	s_waitcnt vmcnt(0)
	ds_write_b128 v124, v[28:31] offset:49152
